# speedup vs baseline: 1.0086x; 1.0046x over previous
.LBB2_24:
	s_or_b64 exec, exec, s[0:1]
	v_and_b32_e32 v1, 31, v0
	v_lshlrev_b32_e32 v2, 2, v1
	v_lshl_or_b32 v2, s10, 7, v2
	v_or_b32_e32 v2, 0x1ee00, v2
	v_lshrrev_b32_e32 v158, 5, v156
	s_waitcnt lgkmcnt(0)
	s_barrier
	v_lshlrev_b32_e32 v250, 4, v158
	v_lshl_or_b32 v250, s10, 7, v250
	v_or_b32_e32 v254, 0x1ee00, v250
	ds_read_b128 v[168:171], v254 offset:0
	ds_read_b128 v[172:175], v254 offset:32
	ds_read_b128 v[176:179], v254 offset:64
	ds_read_b128 v[180:183], v254 offset:96
	v_bfe_u32 v255, v156, 2, 2
	v_lshl_add_u32 v250, v255, 2, v250
	v_add_u32_e32 v250, 0x1e400, v250
	s_waitcnt lgkmcnt(0)
	s_barrier
	ds_read_b32 v157, v2
	v_mul_u32_u24_e32 v2, 0x88, v1
	s_mul_i32 s0, s11, 0x4400
	v_lshlrev_b32_e32 v2, 1, v2
	v_lshlrev_b32_e32 v3, 4, v158
	v_mov_b32_e32 v138, v0
	v_add3_u32 v159, s0, v2, v3
	ds_read_b128 v[2:5], v159
	ds_read_b128 v[18:21], v159 offset:8704
	ds_read_b128 v[130:133], v159 offset:32
	s_waitcnt vmcnt(10) lgkmcnt(2)
	v_mfma_f32_32x32x16_f16 v[50:65], v[2:5], v[126:129], 0
	s_mov_b32 s4, 0xc060c00
	s_mov_b32 s5, 0xe400
	s_mulk_i32 s11, 0x2400
	s_lshl_b32 s0, s10, 6
	s_or_b32 s0, s11, s0
	s_add_i32 s0, s0, 0x11000
	v_mul_u32_u24_e32 v251, 0x90, v1
	v_lshl_add_u32 v251, v158, 3, v251
	v_add_u32_e32 v251, s0, v251
	s_waitcnt lgkmcnt(1)
	v_mfma_f32_32x32x16_f16 v[34:49], v[18:21], v[126:129], 0
	s_or_b32 s0, s8, 2
	s_ashr_i32 s1, s0, 31
	s_lshl_b64 s[0:1], s[0:1], 12
	s_add_u32 s0, s2, s0
	s_addc_u32 s1, s3, s1
	v_cmp_gt_u32_e32 vcc, 32, v156
	v_mfma_f32_32x32x16_f16 v[2:17], v[122:125], v[2:5], v[168:183]
	v_mfma_f32_32x32x16_f16 v[18:33], v[122:125], v[18:21], v[168:183]
	ds_read_b128 v[134:137], v159 offset:8736
	ds_read_b128 v[160:163], v159 offset:64
	s_waitcnt vmcnt(8) lgkmcnt(2)
	v_mfma_f32_32x32x16_f16 v[50:65], v[130:133], v[118:121], v[50:65]
	s_waitcnt lgkmcnt(1)
	v_mfma_f32_32x32x16_f16 v[34:49], v[134:137], v[118:121], v[34:49]
	v_mfma_f32_32x32x16_f16 v[2:17], v[114:117], v[130:133], v[2:17]
	v_mfma_f32_32x32x16_f16 v[18:33], v[114:117], v[134:137], v[18:33]
	ds_read_b128 v[130:133], v159 offset:8768
	ds_read_b128 v[134:137], v159 offset:96
	s_waitcnt vmcnt(6) lgkmcnt(2)
	v_mfma_f32_32x32x16_f16 v[50:65], v[160:163], v[110:113], v[50:65]
	s_waitcnt lgkmcnt(1)
	v_mfma_f32_32x32x16_f16 v[34:49], v[130:133], v[110:113], v[34:49]
	v_mfma_f32_32x32x16_f16 v[2:17], v[106:109], v[160:163], v[2:17]
	v_mfma_f32_32x32x16_f16 v[18:33], v[106:109], v[130:133], v[18:33]
	ds_read_b128 v[130:133], v159 offset:8800
	ds_read_b128 v[160:163], v159 offset:128
	s_waitcnt vmcnt(4) lgkmcnt(2)
	v_mfma_f32_32x32x16_f16 v[50:65], v[134:137], v[102:105], v[50:65]
	s_waitcnt lgkmcnt(1)
	v_mfma_f32_32x32x16_f16 v[34:49], v[130:133], v[102:105], v[34:49]
	v_mfma_f32_32x32x16_f16 v[2:17], v[98:101], v[134:137], v[2:17]
	v_mfma_f32_32x32x16_f16 v[18:33], v[98:101], v[130:133], v[18:33]
	ds_read_b128 v[130:133], v159 offset:8832
	ds_read_b128 v[134:137], v159 offset:160
	s_waitcnt vmcnt(3) lgkmcnt(2)
	v_mfma_f32_32x32x16_f16 v[50:65], v[160:163], v[94:97], v[50:65]
	s_waitcnt lgkmcnt(1)
	v_mfma_f32_32x32x16_f16 v[34:49], v[130:133], v[94:97], v[34:49]
	v_mfma_f32_32x32x16_f16 v[2:17], v[86:89], v[160:163], v[2:17]
	v_mfma_f32_32x32x16_f16 v[18:33], v[86:89], v[130:133], v[18:33]
	ds_read_b128 v[130:133], v159 offset:8864
	ds_read_b128 v[160:163], v159 offset:192
	s_waitcnt vmcnt(2) lgkmcnt(2)
	v_mfma_f32_32x32x16_f16 v[50:65], v[134:137], v[90:93], v[50:65]
	s_waitcnt lgkmcnt(1)
	v_mfma_f32_32x32x16_f16 v[34:49], v[130:133], v[90:93], v[34:49]
	v_mfma_f32_32x32x16_f16 v[2:17], v[78:81], v[134:137], v[2:17]
	v_mfma_f32_32x32x16_f16 v[18:33], v[78:81], v[130:133], v[18:33]
	ds_read_b128 v[130:133], v159 offset:8896
	ds_read_b128 v[164:167], v159 offset:224
	s_waitcnt vmcnt(1) lgkmcnt(2)
	v_mfma_f32_32x32x16_f16 v[50:65], v[160:163], v[82:85], v[50:65]
	s_waitcnt lgkmcnt(1)
	v_mfma_f32_32x32x16_f16 v[34:49], v[130:133], v[82:85], v[34:49]
	v_mfma_f32_32x32x16_f16 v[2:17], v[70:73], v[160:163], v[2:17]
	v_mfma_f32_32x32x16_f16 v[18:33], v[70:73], v[130:133], v[18:33]
	v_lshlrev_b32_e32 v130, 3, v138
	v_and_b32_e32 v241, 0x1f8, v130
	global_load_dwordx2 v[138:139], v241, s[0:1]
	global_load_dwordx2 v[134:135], v241, s[0:1] offset:512
	global_load_dwordx2 v[132:133], v241, s[0:1] offset:1024
	global_load_dwordx2 v[130:131], v241, s[0:1] offset:1536
	global_load_dwordx2 v[136:137], v241, s[0:1] offset:2048
	s_waitcnt vmcnt(5) lgkmcnt(0)
	v_mfma_f32_32x32x16_f16 v[50:65], v[164:167], v[74:77], v[50:65]
	v_mfma_f32_32x32x16_f16 v[2:17], v[66:69], v[164:167], v[2:17]
	s_nop 10
	v_cvt_pk_f16_f32 v57, v56, v57
	v_cvt_pk_f16_f32 v56, v54, v55
	v_cvt_pk_f16_f32 v55, v52, v53
	v_cvt_pk_f16_f32 v54, v50, v51
	v_perm_b32 v50, v240, v154, s42
	v_perm_b32 v51, v240, v154, s43
	v_perm_b32 v52, v240, v155, s42
	v_perm_b32 v53, v240, v155, s43
	v_pk_add_f16 v50, v50, s5 op_sel_hi:[1,0]
	v_pk_add_f16 v51, v51, s5 op_sel_hi:[1,0]
	v_pk_add_f16 v52, v52, s5 op_sel_hi:[1,0]
	v_pk_add_f16 v53, v53, s5 op_sel_hi:[1,0]
	v_cvt_pk_f16_f32 v65, v64, v65
	v_cvt_pk_f16_f32 v64, v62, v63
	v_cvt_pk_f16_f32 v63, v60, v61
	v_cvt_pk_f16_f32 v62, v58, v59
	v_mfma_f32_32x32x16_f16 v[2:17], v[54:57], v[50:53], v[2:17]
	v_perm_b32 v58, v240, v150, s42
	v_perm_b32 v59, v240, v150, s43
	v_perm_b32 v60, v240, v151, s42
	v_perm_b32 v61, v240, v151, s43
	v_pk_add_f16 v58, v58, s5 op_sel_hi:[1,0]
	v_pk_add_f16 v59, v59, s5 op_sel_hi:[1,0]
	v_pk_add_f16 v60, v60, s5 op_sel_hi:[1,0]
	v_pk_add_f16 v61, v61, s5 op_sel_hi:[1,0]
	s_nop 1
	v_mfma_f32_32x32x16_f16 v[2:17], v[62:65], v[58:61], v[2:17]
	ds_read_b128 v[160:163], v159 offset:8928
	v_perm_b32 v155, v240, v152, s43
	v_perm_b32 v164, v240, v153, s42
	s_waitcnt lgkmcnt(0)
	v_mfma_f32_32x32x16_f16 v[18:33], v[66:69], v[160:163], v[18:33]
	v_perm_b32 v154, v240, v152, s42
	v_perm_b32 v165, v240, v153, s43
	v_pk_add_f16 v152, v154, s5 op_sel_hi:[1,0]
	v_pk_add_f16 v153, v155, s5 op_sel_hi:[1,0]
	v_pk_add_f16 v154, v164, s5 op_sel_hi:[1,0]
	v_pk_add_f16 v155, v165, s5 op_sel_hi:[1,0]
	v_mfma_f32_32x32x16_f16 v[34:49], v[160:163], v[74:77], v[34:49]
	v_perm_b32 v151, v240, v148, s43
	v_perm_b32 v164, v240, v149, s42
	v_mfma_f32_32x32x16_f16 v[18:33], v[54:57], v[152:155], v[18:33]
	v_perm_b32 v150, v240, v148, s42
	v_perm_b32 v165, v240, v149, s43
	v_pk_add_f16 v148, v150, s5 op_sel_hi:[1,0]
	v_pk_add_f16 v149, v151, s5 op_sel_hi:[1,0]
	v_pk_add_f16 v150, v164, s5 op_sel_hi:[1,0]
	v_pk_add_f16 v151, v165, s5 op_sel_hi:[1,0]
	s_nop 2
	v_cvt_pk_f16_f32 v41, v40, v41
	v_cvt_pk_f16_f32 v40, v38, v39
	v_cvt_pk_f16_f32 v38, v34, v35
	v_cvt_pk_f16_f32 v39, v36, v37
	v_mfma_f32_32x32x16_f16 v[18:33], v[62:65], v[148:151], v[18:33]
	v_perm_b32 v34, v240, v146, s42
	v_perm_b32 v35, v240, v146, s43
	v_perm_b32 v36, v240, v147, s42
	v_perm_b32 v37, v240, v147, s43
	v_pk_add_f16 v34, v34, s5 op_sel_hi:[1,0]
	v_pk_add_f16 v35, v35, s5 op_sel_hi:[1,0]
	v_pk_add_f16 v36, v36, s5 op_sel_hi:[1,0]
	v_pk_add_f16 v37, v37, s5 op_sel_hi:[1,0]
	v_perm_b32 v146, v240, v144, s42
	v_perm_b32 v144, v240, v144, s43
	v_perm_b32 v147, v240, v145, s42
	v_perm_b32 v53, v240, v145, s43
	v_pk_add_f16 v50, v146, s5 op_sel_hi:[1,0]
	v_pk_add_f16 v51, v144, s5 op_sel_hi:[1,0]
	v_pk_add_f16 v52, v147, s5 op_sel_hi:[1,0]
	v_pk_add_f16 v53, v53, s5 op_sel_hi:[1,0]
	v_cvt_pk_f16_f32 v49, v48, v49
	v_cvt_pk_f16_f32 v48, v46, v47
	v_cvt_pk_f16_f32 v47, v44, v45
	v_mfma_f32_32x32x16_f16 v[2:17], v[38:41], v[34:37], v[2:17]
	v_cvt_pk_f16_f32 v46, v42, v43
	v_mfma_f32_32x32x16_f16 v[18:33], v[38:41], v[50:53], v[18:33]
	v_perm_b32 v34, v240, v140, s42
	v_perm_b32 v35, v240, v140, s43
	v_perm_b32 v36, v240, v141, s42
	v_perm_b32 v37, v240, v141, s43
	v_perm_b32 v42, v240, v142, s42
	v_perm_b32 v43, v240, v142, s43
	v_perm_b32 v44, v240, v143, s42
	v_perm_b32 v45, v240, v143, s43
	v_pk_add_f16 v34, v34, s5 op_sel_hi:[1,0]
	v_pk_add_f16 v35, v35, s5 op_sel_hi:[1,0]
	v_pk_add_f16 v36, v36, s5 op_sel_hi:[1,0]
	v_pk_add_f16 v37, v37, s5 op_sel_hi:[1,0]
	v_pk_add_f16 v42, v42, s5 op_sel_hi:[1,0]
	v_pk_add_f16 v43, v43, s5 op_sel_hi:[1,0]
	v_pk_add_f16 v44, v44, s5 op_sel_hi:[1,0]
	v_pk_add_f16 v45, v45, s5 op_sel_hi:[1,0]
	v_mfma_f32_32x32x16_f16 v[18:33], v[46:49], v[34:37], v[18:33]
	global_load_dwordx2 v[154:155], v241, s[0:1] offset:2560
	global_load_dwordx2 v[152:153], v241, s[0:1] offset:3072
	global_load_dwordx2 v[150:151], v241, s[0:1] offset:3584
	v_mov_b32_e32 v148, v0
	s_or_b32 s0, s8, 4
	s_ashr_i32 s1, s0, 31
	s_lshl_b64 s[0:1], s[0:1], 12
	v_mfma_f32_32x32x16_f16 v[2:17], v[46:49], v[42:45], v[2:17]
	s_nop 7
	s_nop 4
	v_cvt_pk_f16_f32 v254, v2, v3
	v_cvt_pk_f16_f32 v255, v4, v5
	ds_write_b64 v251, v[254:255] offset:0
	v_cvt_pk_f16_f32 v252, v6, v7
	v_cvt_pk_f16_f32 v253, v8, v9
	ds_write_b64 v251, v[252:253] offset:16
	v_cvt_pk_f16_f32 v254, v10, v11
	v_cvt_pk_f16_f32 v255, v12, v13
	ds_write_b64 v251, v[254:255] offset:32
	v_cvt_pk_f16_f32 v252, v14, v15
	v_cvt_pk_f16_f32 v253, v16, v17
	ds_write_b64 v251, v[252:253] offset:48
	v_cvt_pk_f16_f32 v254, v18, v19
	v_cvt_pk_f16_f32 v255, v20, v21
	ds_write_b64 v251, v[254:255] offset:4608
	v_pk_add_f32 v[222:223], v[2:3], v[18:19]
	v_pk_mul_f32 v[194:195], v[2:3], v[2:3]
	v_pk_fma_f32 v[194:195], v[18:19], v[18:19], v[194:195]
	v_pk_add_f32 v[220:221], v[4:5], v[20:21]
	v_pk_mul_f32 v[192:193], v[4:5], v[4:5]
	v_pk_fma_f32 v[192:193], v[20:21], v[20:21], v[192:193]
	v_cvt_pk_f16_f32 v252, v22, v23
	v_cvt_pk_f16_f32 v253, v24, v25
	ds_write_b64 v251, v[252:253] offset:4624
	v_pk_add_f32 v[218:219], v[6:7], v[22:23]
	v_pk_mul_f32 v[184:185], v[6:7], v[6:7]
	v_pk_fma_f32 v[184:185], v[22:23], v[22:23], v[184:185]
	v_pk_add_f32 v[216:217], v[8:9], v[24:25]
	v_pk_mul_f32 v[166:167], v[8:9], v[8:9]
	v_pk_fma_f32 v[166:167], v[24:25], v[24:25], v[166:167]
	v_cvt_pk_f16_f32 v254, v26, v27
	v_cvt_pk_f16_f32 v255, v28, v29
	ds_write_b64 v251, v[254:255] offset:4640
	v_pk_add_f32 v[214:215], v[10:11], v[26:27]
	v_pk_mul_f32 v[164:165], v[10:11], v[10:11]
	v_pk_fma_f32 v[164:165], v[26:27], v[26:27], v[164:165]
	v_pk_add_f32 v[204:205], v[12:13], v[28:29]
	v_pk_mul_f32 v[162:163], v[12:13], v[12:13]
	v_pk_fma_f32 v[162:163], v[28:29], v[28:29], v[162:163]
	v_cvt_pk_f16_f32 v252, v30, v31
	v_cvt_pk_f16_f32 v253, v32, v33
	ds_write_b64 v251, v[252:253] offset:4656
	v_pk_add_f32 v[202:203], v[14:15], v[30:31]
	v_pk_mul_f32 v[160:161], v[14:15], v[14:15]
	v_pk_fma_f32 v[160:161], v[30:31], v[30:31], v[160:161]
	v_pk_add_f32 v[196:197], v[16:17], v[32:33]
	v_pk_mul_f32 v[156:157], v[16:17], v[16:17]
	v_pk_fma_f32 v[156:157], v[32:33], v[32:33], v[156:157]
	s_nop 3
	s_nop 0
	s_waitcnt lgkmcnt(0)
	s_barrier
	s_nop 4
	ds_read_b128 v[2:5], v159 offset:34816
	ds_read_b128 v[18:21], v159 offset:43520
	ds_read_b128 v[140:143], v159 offset:34848
	ds_read_b128 v[144:147], v159 offset:43552
	s_waitcnt lgkmcnt(3)
	v_mfma_f32_32x32x16_f16 v[50:65], v[2:5], v[126:129], 0
	s_add_u32 s0, s2, s0
	s_addc_u32 s1, s3, s1
	s_waitcnt lgkmcnt(2)
	v_mfma_f32_32x32x16_f16 v[34:49], v[18:21], v[126:129], 0
	v_mfma_f32_32x32x16_f16 v[2:17], v[122:125], v[2:5], v[168:183]
	v_mfma_f32_32x32x16_f16 v[18:33], v[122:125], v[18:21], v[168:183]
	ds_read_b128 v[242:245], v159 offset:34880
	ds_read_b128 v[246:249], v159 offset:43584
	s_waitcnt lgkmcnt(3)
	v_mfma_f32_32x32x16_f16 v[50:65], v[140:143], v[118:121], v[50:65]
	s_waitcnt lgkmcnt(2)
	v_mfma_f32_32x32x16_f16 v[34:49], v[144:147], v[118:121], v[34:49]
	v_mfma_f32_32x32x16_f16 v[2:17], v[114:117], v[140:143], v[2:17]
	v_mfma_f32_32x32x16_f16 v[18:33], v[114:117], v[144:147], v[18:33]
	ds_read_b128 v[140:143], v159 offset:34912
	ds_read_b128 v[144:147], v159 offset:43616
	s_waitcnt lgkmcnt(3)
	v_mfma_f32_32x32x16_f16 v[50:65], v[242:245], v[110:113], v[50:65]
	s_waitcnt lgkmcnt(2)
	v_mfma_f32_32x32x16_f16 v[34:49], v[246:249], v[110:113], v[34:49]
	v_mfma_f32_32x32x16_f16 v[2:17], v[106:109], v[242:245], v[2:17]
	v_mfma_f32_32x32x16_f16 v[18:33], v[106:109], v[246:249], v[18:33]
	ds_read_b128 v[242:245], v159 offset:34944
	ds_read_b128 v[246:249], v159 offset:43648
	s_waitcnt lgkmcnt(3)
	v_mfma_f32_32x32x16_f16 v[50:65], v[140:143], v[102:105], v[50:65]
	s_waitcnt lgkmcnt(2)
	v_mfma_f32_32x32x16_f16 v[34:49], v[144:147], v[102:105], v[34:49]
	v_mfma_f32_32x32x16_f16 v[2:17], v[98:101], v[140:143], v[2:17]
	v_mfma_f32_32x32x16_f16 v[18:33], v[98:101], v[144:147], v[18:33]
	ds_read_b128 v[186:189], v159 offset:34976
	ds_read_b128 v[206:209], v159 offset:43680
	s_waitcnt lgkmcnt(3)
	v_mfma_f32_32x32x16_f16 v[50:65], v[242:245], v[94:97], v[50:65]
	s_waitcnt lgkmcnt(2)
	v_mfma_f32_32x32x16_f16 v[34:49], v[246:249], v[94:97], v[34:49]
	v_mfma_f32_32x32x16_f16 v[2:17], v[86:89], v[242:245], v[2:17]
	v_mfma_f32_32x32x16_f16 v[18:33], v[86:89], v[246:249], v[18:33]
	ds_read_b128 v[140:143], v159 offset:35008
	ds_read_b128 v[144:147], v159 offset:43712
	s_waitcnt lgkmcnt(3)
	v_mfma_f32_32x32x16_f16 v[50:65], v[186:189], v[90:93], v[50:65]
	s_waitcnt lgkmcnt(2)
	v_mfma_f32_32x32x16_f16 v[34:49], v[206:209], v[90:93], v[34:49]
	v_mfma_f32_32x32x16_f16 v[2:17], v[78:81], v[186:189], v[2:17]
	v_mfma_f32_32x32x16_f16 v[18:33], v[78:81], v[206:209], v[18:33]
	ds_read_b128 v[186:189], v159 offset:35040
	ds_read_b128 v[206:209], v159 offset:43744
	s_waitcnt lgkmcnt(3)
	v_mfma_f32_32x32x16_f16 v[50:65], v[140:143], v[82:85], v[50:65]
	s_waitcnt lgkmcnt(2)
	v_mfma_f32_32x32x16_f16 v[34:49], v[144:147], v[82:85], v[34:49]
	v_mfma_f32_32x32x16_f16 v[2:17], v[70:73], v[140:143], v[2:17]
	v_lshlrev_b32_e32 v140, 3, v148
	v_and_b32_e32 v199, 0x1f8, v140
	global_load_dwordx2 v[148:149], v199, s[0:1]
	global_load_dwordx2 v[142:143], v199, s[0:1] offset:1024
	global_load_dwordx2 v[140:141], v199, s[0:1] offset:1536
	v_mfma_f32_32x32x16_f16 v[18:33], v[70:73], v[144:147], v[18:33]
	global_load_dwordx2 v[144:145], v199, s[0:1] offset:512
	global_load_dwordx2 v[146:147], v199, s[0:1] offset:2048
	s_waitcnt lgkmcnt(1)
	v_mfma_f32_32x32x16_f16 v[50:65], v[186:189], v[74:77], v[50:65]
	v_mfma_f32_32x32x16_f16 v[2:17], v[66:69], v[186:189], v[2:17]
	s_nop 10
	v_cvt_pk_f16_f32 v57, v56, v57
	v_cvt_pk_f16_f32 v56, v54, v55
	v_cvt_pk_f16_f32 v54, v50, v51
	s_waitcnt vmcnt(12)
	v_cvt_pk_f16_f32 v55, v52, v53
	s_waitcnt vmcnt(8)
	v_perm_b32 v50, v240, v138, s42
	v_perm_b32 v51, v240, v138, s43
	v_perm_b32 v52, v240, v139, s42
	v_perm_b32 v53, v240, v139, s43
	v_perm_b32 v139, v240, v136, s43
	v_pk_add_f16 v50, v50, s5 op_sel_hi:[1,0]
	v_pk_add_f16 v51, v51, s5 op_sel_hi:[1,0]
	v_pk_add_f16 v52, v52, s5 op_sel_hi:[1,0]
	v_pk_add_f16 v53, v53, s5 op_sel_hi:[1,0]
	v_perm_b32 v190, v240, v137, s42
	s_waitcnt lgkmcnt(0)
	v_mfma_f32_32x32x16_f16 v[18:33], v[66:69], v[206:209], v[18:33]
	v_perm_b32 v138, v240, v136, s42
	v_perm_b32 v191, v240, v137, s43
	v_pk_add_f16 v136, v138, s5 op_sel_hi:[1,0]
	v_pk_add_f16 v137, v139, s5 op_sel_hi:[1,0]
	v_pk_add_f16 v138, v190, s5 op_sel_hi:[1,0]
	v_pk_add_f16 v139, v191, s5 op_sel_hi:[1,0]
	v_cvt_pk_f16_f32 v65, v64, v65
	v_cvt_pk_f16_f32 v64, v62, v63
	v_cvt_pk_f16_f32 v63, v60, v61
	v_cvt_pk_f16_f32 v62, v58, v59
	v_mfma_f32_32x32x16_f16 v[34:49], v[206:209], v[74:77], v[34:49]
	v_mfma_f32_32x32x16_f16 v[2:17], v[54:57], v[50:53], v[2:17]
	s_waitcnt vmcnt(7)
	v_perm_b32 v58, v240, v134, s42
	v_perm_b32 v59, v240, v134, s43
	v_perm_b32 v60, v240, v135, s42
	v_perm_b32 v61, v240, v135, s43
	v_pk_add_f16 v58, v58, s5 op_sel_hi:[1,0]
	v_pk_add_f16 v59, v59, s5 op_sel_hi:[1,0]
	v_pk_add_f16 v60, v60, s5 op_sel_hi:[1,0]
	v_pk_add_f16 v61, v61, s5 op_sel_hi:[1,0]
	v_mfma_f32_32x32x16_f16 v[18:33], v[54:57], v[136:139], v[18:33]
	v_perm_b32 v134, v240, v154, s42
	v_perm_b32 v135, v240, v154, s43
	v_perm_b32 v154, v240, v155, s42
	v_perm_b32 v155, v240, v155, s43
	v_pk_add_f16 v210, v134, s5 op_sel_hi:[1,0]
	v_pk_add_f16 v211, v135, s5 op_sel_hi:[1,0]
	v_pk_add_f16 v212, v154, s5 op_sel_hi:[1,0]
	v_pk_add_f16 v213, v155, s5 op_sel_hi:[1,0]
	v_cvt_pk_f16_f32 v41, v40, v41
	v_cvt_pk_f16_f32 v40, v38, v39
	v_cvt_pk_f16_f32 v39, v36, v37
	v_cvt_pk_f16_f32 v38, v34, v35
	v_mfma_f32_32x32x16_f16 v[2:17], v[62:65], v[58:61], v[2:17]
	v_perm_b32 v34, v240, v132, s42
	v_perm_b32 v35, v240, v132, s43
	v_perm_b32 v36, v240, v133, s42
	v_perm_b32 v37, v240, v133, s43
	v_pk_add_f16 v34, v34, s5 op_sel_hi:[1,0]
	v_pk_add_f16 v35, v35, s5 op_sel_hi:[1,0]
	v_pk_add_f16 v36, v36, s5 op_sel_hi:[1,0]
	v_pk_add_f16 v37, v37, s5 op_sel_hi:[1,0]
	s_waitcnt vmcnt(6)
	v_mfma_f32_32x32x16_f16 v[18:33], v[62:65], v[210:213], v[18:33]
	v_perm_b32 v132, v240, v152, s42
	v_perm_b32 v133, v240, v152, s43
	v_perm_b32 v134, v240, v153, s42
	v_perm_b32 v53, v240, v153, s43
	v_pk_add_f16 v50, v132, s5 op_sel_hi:[1,0]
	v_pk_add_f16 v51, v133, s5 op_sel_hi:[1,0]
	v_pk_add_f16 v52, v134, s5 op_sel_hi:[1,0]
	v_pk_add_f16 v53, v53, s5 op_sel_hi:[1,0]
	v_cvt_pk_f16_f32 v49, v48, v49
	v_cvt_pk_f16_f32 v48, v46, v47
	v_cvt_pk_f16_f32 v47, v44, v45
	v_cvt_pk_f16_f32 v46, v42, v43
	v_mfma_f32_32x32x16_f16 v[2:17], v[38:41], v[34:37], v[2:17]
	v_perm_b32 v42, v240, v130, s42
	v_perm_b32 v43, v240, v130, s43
	v_perm_b32 v44, v240, v131, s42
	v_perm_b32 v45, v240, v131, s43
	v_pk_add_f16 v42, v42, s5 op_sel_hi:[1,0]
	v_pk_add_f16 v43, v43, s5 op_sel_hi:[1,0]
	v_pk_add_f16 v44, v44, s5 op_sel_hi:[1,0]
	v_pk_add_f16 v45, v45, s5 op_sel_hi:[1,0]
	s_waitcnt vmcnt(5)
	v_mfma_f32_32x32x16_f16 v[18:33], v[38:41], v[50:53], v[18:33]
	v_perm_b32 v34, v240, v150, s42
	v_perm_b32 v35, v240, v150, s43
	v_perm_b32 v36, v240, v151, s42
	v_perm_b32 v37, v240, v151, s43
	v_pk_add_f16 v34, v34, s5 op_sel_hi:[1,0]
	v_pk_add_f16 v35, v35, s5 op_sel_hi:[1,0]
	v_pk_add_f16 v36, v36, s5 op_sel_hi:[1,0]
	v_pk_add_f16 v37, v37, s5 op_sel_hi:[1,0]
	v_mfma_f32_32x32x16_f16 v[2:17], v[46:49], v[42:45], v[2:17]
	global_load_dwordx2 v[154:155], v199, s[0:1] offset:2560
	global_load_dwordx2 v[152:153], v199, s[0:1] offset:3072
	global_load_dwordx2 v[150:151], v199, s[0:1] offset:3584
	s_or_b32 s0, s8, 6
	s_ashr_i32 s1, s0, 31
	s_lshl_b64 s[0:1], s[0:1], 12
	s_add_u32 s0, s2, s0
	v_mfma_f32_32x32x16_f16 v[18:33], v[46:49], v[34:37], v[18:33]
	s_nop 7
	s_nop 4
	v_cvt_pk_f16_f32 v254, v2, v3
	v_cvt_pk_f16_f32 v255, v4, v5
	ds_write_b64 v251, v[254:255] offset:18432
	v_pk_add_f32 v[222:223], v[222:223], v[2:3]
	v_pk_fma_f32 v[194:195], v[2:3], v[2:3], v[194:195]
	v_pk_add_f32 v[220:221], v[220:221], v[4:5]
	v_pk_fma_f32 v[192:193], v[4:5], v[4:5], v[192:193]
	v_cvt_pk_f16_f32 v252, v6, v7
	v_cvt_pk_f16_f32 v253, v8, v9
	ds_write_b64 v251, v[252:253] offset:18448
	v_pk_add_f32 v[218:219], v[218:219], v[6:7]
	v_pk_fma_f32 v[184:185], v[6:7], v[6:7], v[184:185]
	v_pk_add_f32 v[216:217], v[216:217], v[8:9]
	v_pk_fma_f32 v[166:167], v[8:9], v[8:9], v[166:167]
	v_cvt_pk_f16_f32 v254, v10, v11
	v_cvt_pk_f16_f32 v255, v12, v13
	ds_write_b64 v251, v[254:255] offset:18464
	v_pk_add_f32 v[214:215], v[214:215], v[10:11]
	v_pk_fma_f32 v[164:165], v[10:11], v[10:11], v[164:165]
	v_pk_add_f32 v[204:205], v[204:205], v[12:13]
	v_pk_fma_f32 v[162:163], v[12:13], v[12:13], v[162:163]
	v_cvt_pk_f16_f32 v252, v14, v15
	v_cvt_pk_f16_f32 v253, v16, v17
	ds_write_b64 v251, v[252:253] offset:18480
	v_pk_add_f32 v[202:203], v[202:203], v[14:15]
	v_pk_fma_f32 v[160:161], v[14:15], v[14:15], v[160:161]
	v_pk_add_f32 v[196:197], v[196:197], v[16:17]
	v_pk_fma_f32 v[156:157], v[16:17], v[16:17], v[156:157]
	v_cvt_pk_f16_f32 v254, v18, v19
	v_cvt_pk_f16_f32 v255, v20, v21
	ds_write_b64 v251, v[254:255] offset:23040
	v_pk_add_f32 v[222:223], v[222:223], v[18:19]
	v_pk_fma_f32 v[194:195], v[18:19], v[18:19], v[194:195]
	v_pk_add_f32 v[220:221], v[220:221], v[20:21]
	v_pk_fma_f32 v[192:193], v[20:21], v[20:21], v[192:193]
	v_cvt_pk_f16_f32 v252, v22, v23
	v_cvt_pk_f16_f32 v253, v24, v25
	ds_write_b64 v251, v[252:253] offset:23056
	v_pk_add_f32 v[218:219], v[218:219], v[22:23]
	v_pk_fma_f32 v[184:185], v[22:23], v[22:23], v[184:185]
	v_pk_add_f32 v[216:217], v[216:217], v[24:25]
	v_pk_fma_f32 v[166:167], v[24:25], v[24:25], v[166:167]
	v_cvt_pk_f16_f32 v254, v26, v27
	v_cvt_pk_f16_f32 v255, v28, v29
	ds_write_b64 v251, v[254:255] offset:23072
	v_pk_add_f32 v[214:215], v[214:215], v[26:27]
	v_pk_fma_f32 v[164:165], v[26:27], v[26:27], v[164:165]
	v_pk_add_f32 v[204:205], v[204:205], v[28:29]
	v_pk_fma_f32 v[162:163], v[28:29], v[28:29], v[162:163]
	v_cvt_pk_f16_f32 v252, v30, v31
	v_cvt_pk_f16_f32 v253, v32, v33
	ds_write_b64 v251, v[252:253] offset:23088
	v_pk_add_f32 v[202:203], v[202:203], v[30:31]
	v_pk_fma_f32 v[160:161], v[30:31], v[30:31], v[160:161]
	v_pk_add_f32 v[196:197], v[196:197], v[32:33]
	v_pk_fma_f32 v[156:157], v[32:33], v[32:33], v[156:157]
	s_nop 3
	s_nop 0
	s_nop 0
	s_waitcnt lgkmcnt(0)
	s_barrier
	ds_read_b128 v[2:5], v159
	s_nop 2
	ds_read_b128 v[18:21], v159 offset:8704
	s_waitcnt lgkmcnt(1)
	v_mfma_f32_32x32x16_f16 v[50:65], v[2:5], v[126:129], 0
	v_lshlrev_b32_e32 v0, 3, v0
	s_addc_u32 s1, s3, s1
	v_and_b32_e32 v0, 0x1f8, v0
	global_load_dwordx2 v[138:139], v0, s[0:1]
	s_waitcnt lgkmcnt(0)
	v_mfma_f32_32x32x16_f16 v[34:49], v[18:21], v[126:129], 0
	v_mfma_f32_32x32x16_f16 v[2:17], v[122:125], v[2:5], v[168:183]
	v_mfma_f32_32x32x16_f16 v[18:33], v[122:125], v[18:21], v[168:183]
	ds_read_b128 v[130:133], v159 offset:32
	ds_read_b128 v[134:137], v159 offset:8736
	s_waitcnt lgkmcnt(1)
	v_mfma_f32_32x32x16_f16 v[50:65], v[130:133], v[118:121], v[50:65]
	s_waitcnt lgkmcnt(0)
	v_mfma_f32_32x32x16_f16 v[34:49], v[134:137], v[118:121], v[34:49]
	v_mfma_f32_32x32x16_f16 v[2:17], v[114:117], v[130:133], v[2:17]
	v_mfma_f32_32x32x16_f16 v[18:33], v[114:117], v[134:137], v[18:33]
	ds_read_b128 v[224:227], v159 offset:64
	ds_read_b128 v[228:231], v159 offset:8768
	ds_read_b128 v[130:133], v159 offset:96
	ds_read_b128 v[134:137], v159 offset:8800
	s_waitcnt lgkmcnt(3)
	v_mfma_f32_32x32x16_f16 v[50:65], v[224:227], v[110:113], v[50:65]
	s_waitcnt lgkmcnt(2)
	v_mfma_f32_32x32x16_f16 v[34:49], v[228:231], v[110:113], v[34:49]
	v_mfma_f32_32x32x16_f16 v[2:17], v[106:109], v[224:227], v[2:17]
	v_mfma_f32_32x32x16_f16 v[18:33], v[106:109], v[228:231], v[18:33]
	ds_read_b128 v[224:227], v159 offset:128
	ds_read_b128 v[228:231], v159 offset:8832
	s_waitcnt lgkmcnt(3)
	v_mfma_f32_32x32x16_f16 v[50:65], v[130:133], v[102:105], v[50:65]
	s_waitcnt lgkmcnt(2)
	v_mfma_f32_32x32x16_f16 v[34:49], v[134:137], v[102:105], v[34:49]
	v_mfma_f32_32x32x16_f16 v[2:17], v[98:101], v[130:133], v[2:17]
	v_mfma_f32_32x32x16_f16 v[18:33], v[98:101], v[134:137], v[18:33]
	ds_read_b128 v[130:133], v159 offset:160
	ds_read_b128 v[134:137], v159 offset:8864
	s_waitcnt lgkmcnt(3)
	v_mfma_f32_32x32x16_f16 v[50:65], v[224:227], v[94:97], v[50:65]
	s_waitcnt lgkmcnt(2)
	v_mfma_f32_32x32x16_f16 v[34:49], v[228:231], v[94:97], v[34:49]
	v_mfma_f32_32x32x16_f16 v[2:17], v[86:89], v[224:227], v[2:17]
	v_mfma_f32_32x32x16_f16 v[18:33], v[86:89], v[228:231], v[18:33]
	ds_read_b128 v[224:227], v159 offset:192
	ds_read_b128 v[228:231], v159 offset:8896
	s_waitcnt lgkmcnt(3)
	v_mfma_f32_32x32x16_f16 v[50:65], v[130:133], v[90:93], v[50:65]
	s_waitcnt lgkmcnt(2)
	v_mfma_f32_32x32x16_f16 v[34:49], v[134:137], v[90:93], v[34:49]
	v_mfma_f32_32x32x16_f16 v[2:17], v[78:81], v[130:133], v[2:17]
	v_mfma_f32_32x32x16_f16 v[18:33], v[78:81], v[134:137], v[18:33]
	ds_read_b128 v[232:235], v159 offset:224
	ds_read_b128 v[236:239], v159 offset:8928
	s_waitcnt lgkmcnt(3)
	v_mfma_f32_32x32x16_f16 v[50:65], v[224:227], v[82:85], v[50:65]
	global_load_dwordx2 v[134:135], v0, s[0:1] offset:512
	global_load_dwordx2 v[132:133], v0, s[0:1] offset:1024
	global_load_dwordx2 v[130:131], v0, s[0:1] offset:1536
	s_waitcnt lgkmcnt(2)
	v_mfma_f32_32x32x16_f16 v[34:49], v[228:231], v[82:85], v[34:49]
	global_load_dwordx2 v[136:137], v0, s[0:1] offset:2048
	v_mfma_f32_32x32x16_f16 v[2:17], v[70:73], v[224:227], v[2:17]
	v_mfma_f32_32x32x16_f16 v[18:33], v[70:73], v[228:231], v[18:33]
	s_waitcnt lgkmcnt(1)
	v_mfma_f32_32x32x16_f16 v[50:65], v[232:235], v[74:77], v[50:65]
	v_mfma_f32_32x32x16_f16 v[2:17], v[66:69], v[232:235], v[2:17]
	s_nop 10
	v_cvt_pk_f16_f32 v57, v56, v57
	v_cvt_pk_f16_f32 v56, v54, v55
	v_cvt_pk_f16_f32 v54, v50, v51
	s_waitcnt vmcnt(12)
	v_lshlrev_b32_e32 v50, 8, v148
	v_cvt_pk_f16_f32 v55, v52, v53
	v_perm_b32 v50, v50, v148, s4
	v_lshrrev_b32_e32 v51, 16, v148
	v_lshrrev_b32_e32 v52, 8, v148
	v_lshrrev_b32_e32 v53, 16, v149
	v_lshrrev_b32_e32 v148, 8, v149
	v_perm_b32 v51, v52, v51, s4
	v_lshlrev_b32_e32 v52, 8, v149
	v_perm_b32 v53, v148, v53, s4
	s_waitcnt vmcnt(8)
	v_perm_b32 v52, v52, v149, s4
	v_perm_b32 v149, v240, v146, s43
	v_perm_b32 v198, v240, v147, s42
	s_waitcnt lgkmcnt(0)
	v_mfma_f32_32x32x16_f16 v[18:33], v[66:69], v[236:239], v[18:33]
	v_or_b32_e32 v50, 0x64006400, v50
	v_or_b32_e32 v51, 0x64006400, v51
	v_or_b32_e32 v52, 0x64006400, v52
	v_or_b32_e32 v53, 0x64006400, v53
	v_pk_add_f16 v50, v50, s5 op_sel_hi:[1,0]
	v_pk_add_f16 v51, v51, s5 op_sel_hi:[1,0]
	v_pk_add_f16 v52, v52, s5 op_sel_hi:[1,0]
	v_pk_add_f16 v53, v53, s5 op_sel_hi:[1,0]
	v_perm_b32 v148, v240, v146, s42
	v_perm_b32 v200, v240, v147, s43
	v_pk_add_f16 v146, v148, s5 op_sel_hi:[1,0]
	v_pk_add_f16 v147, v149, s5 op_sel_hi:[1,0]
	v_pk_add_f16 v148, v198, s5 op_sel_hi:[1,0]
	v_pk_add_f16 v149, v200, s5 op_sel_hi:[1,0]
	v_cvt_pk_f16_f32 v65, v64, v65
	v_cvt_pk_f16_f32 v64, v62, v63
	v_cvt_pk_f16_f32 v62, v58, v59
	v_cvt_pk_f16_f32 v63, v60, v61
	s_waitcnt vmcnt(7)
	v_mfma_f32_32x32x16_f16 v[34:49], v[236:239], v[74:77], v[34:49]
	v_mfma_f32_32x32x16_f16 v[2:17], v[54:57], v[50:53], v[2:17]
	v_perm_b32 v58, v240, v144, s42
	v_perm_b32 v59, v240, v144, s43
	v_perm_b32 v60, v240, v145, s42
	v_perm_b32 v61, v240, v145, s43
	v_mfma_f32_32x32x16_f16 v[18:33], v[54:57], v[146:149], v[18:33]
	v_pk_add_f16 v58, v58, s5 op_sel_hi:[1,0]
	v_pk_add_f16 v59, v59, s5 op_sel_hi:[1,0]
	v_pk_add_f16 v60, v60, s5 op_sel_hi:[1,0]
	v_pk_add_f16 v61, v61, s5 op_sel_hi:[1,0]
	v_perm_b32 v144, v240, v154, s42
	v_perm_b32 v145, v240, v154, s43
	v_perm_b32 v154, v240, v155, s42
	v_perm_b32 v155, v240, v155, s43
	v_pk_add_f16 v224, v144, s5 op_sel_hi:[1,0]
	v_pk_add_f16 v225, v145, s5 op_sel_hi:[1,0]
	v_pk_add_f16 v226, v154, s5 op_sel_hi:[1,0]
	v_pk_add_f16 v227, v155, s5 op_sel_hi:[1,0]
	v_cvt_pk_f16_f32 v41, v40, v41
	v_cvt_pk_f16_f32 v40, v38, v39
	v_cvt_pk_f16_f32 v39, v36, v37
	v_cvt_pk_f16_f32 v38, v34, v35
	s_waitcnt vmcnt(6)
	v_mfma_f32_32x32x16_f16 v[2:17], v[62:65], v[58:61], v[2:17]
	v_perm_b32 v34, v240, v142, s42
	v_perm_b32 v35, v240, v142, s43
	v_mfma_f32_32x32x16_f16 v[18:33], v[62:65], v[224:227], v[18:33]
	v_perm_b32 v36, v240, v143, s42
	v_perm_b32 v37, v240, v143, s43
	v_pk_add_f16 v34, v34, s5 op_sel_hi:[1,0]
	v_pk_add_f16 v35, v35, s5 op_sel_hi:[1,0]
	v_pk_add_f16 v36, v36, s5 op_sel_hi:[1,0]
	v_pk_add_f16 v37, v37, s5 op_sel_hi:[1,0]
	v_perm_b32 v142, v240, v152, s42
	v_perm_b32 v143, v240, v152, s43
	v_perm_b32 v144, v240, v153, s42
	v_perm_b32 v53, v240, v153, s43
	v_pk_add_f16 v50, v142, s5 op_sel_hi:[1,0]
	v_pk_add_f16 v51, v143, s5 op_sel_hi:[1,0]
	v_pk_add_f16 v52, v144, s5 op_sel_hi:[1,0]
	v_pk_add_f16 v53, v53, s5 op_sel_hi:[1,0]
	v_cvt_pk_f16_f32 v49, v48, v49
	v_cvt_pk_f16_f32 v48, v46, v47
	v_cvt_pk_f16_f32 v47, v44, v45
	v_cvt_pk_f16_f32 v46, v42, v43
	v_mfma_f32_32x32x16_f16 v[2:17], v[38:41], v[34:37], v[2:17]
	s_waitcnt vmcnt(5)
	v_mfma_f32_32x32x16_f16 v[18:33], v[38:41], v[50:53], v[18:33]
	v_perm_b32 v42, v240, v140, s42
	v_perm_b32 v43, v240, v140, s43
	v_perm_b32 v44, v240, v141, s42
	v_perm_b32 v45, v240, v141, s43
	v_perm_b32 v34, v240, v150, s42
	v_perm_b32 v35, v240, v150, s43
	v_perm_b32 v36, v240, v151, s42
	v_perm_b32 v37, v240, v151, s43
	v_pk_add_f16 v42, v42, s5 op_sel_hi:[1,0]
	v_pk_add_f16 v43, v43, s5 op_sel_hi:[1,0]
	v_pk_add_f16 v44, v44, s5 op_sel_hi:[1,0]
	v_pk_add_f16 v45, v45, s5 op_sel_hi:[1,0]
	v_pk_add_f16 v34, v34, s5 op_sel_hi:[1,0]
	v_pk_add_f16 v35, v35, s5 op_sel_hi:[1,0]
	v_pk_add_f16 v36, v36, s5 op_sel_hi:[1,0]
	v_pk_add_f16 v37, v37, s5 op_sel_hi:[1,0]
	v_mfma_f32_32x32x16_f16 v[2:17], v[46:49], v[42:45], v[2:17]
	global_load_dwordx2 v[142:143], v0, s[0:1] offset:2560
	global_load_dwordx2 v[140:141], v0, s[0:1] offset:3072
	global_load_dwordx2 v[64:65], v0, s[0:1] offset:3584
	v_mfma_f32_32x32x16_f16 v[18:33], v[46:49], v[34:37], v[18:33]
	s_nop 7
	s_nop 4
	v_cvt_pk_f16_f32 v254, v2, v3
	v_cvt_pk_f16_f32 v255, v4, v5
	ds_write_b64 v251, v[254:255] offset:0
	v_pk_add_f32 v[222:223], v[222:223], v[2:3]
	v_pk_fma_f32 v[194:195], v[2:3], v[2:3], v[194:195]
	v_pk_add_f32 v[220:221], v[220:221], v[4:5]
	v_pk_fma_f32 v[192:193], v[4:5], v[4:5], v[192:193]
	v_cvt_pk_f16_f32 v252, v6, v7
	v_cvt_pk_f16_f32 v253, v8, v9
	ds_write_b64 v251, v[252:253] offset:16
	v_pk_add_f32 v[218:219], v[218:219], v[6:7]
	v_pk_fma_f32 v[184:185], v[6:7], v[6:7], v[184:185]
	v_pk_add_f32 v[216:217], v[216:217], v[8:9]
	v_pk_fma_f32 v[166:167], v[8:9], v[8:9], v[166:167]
	v_cvt_pk_f16_f32 v254, v10, v11
	v_cvt_pk_f16_f32 v255, v12, v13
	ds_write_b64 v251, v[254:255] offset:32
	v_pk_add_f32 v[214:215], v[214:215], v[10:11]
	v_pk_fma_f32 v[164:165], v[10:11], v[10:11], v[164:165]
	v_pk_add_f32 v[204:205], v[204:205], v[12:13]
	v_pk_fma_f32 v[162:163], v[12:13], v[12:13], v[162:163]
	v_cvt_pk_f16_f32 v252, v14, v15
	v_cvt_pk_f16_f32 v253, v16, v17
	ds_write_b64 v251, v[252:253] offset:48
	v_pk_add_f32 v[202:203], v[202:203], v[14:15]
	v_pk_fma_f32 v[160:161], v[14:15], v[14:15], v[160:161]
	v_pk_add_f32 v[196:197], v[196:197], v[16:17]
	v_pk_fma_f32 v[156:157], v[16:17], v[16:17], v[156:157]
	v_cvt_pk_f16_f32 v254, v18, v19
	v_cvt_pk_f16_f32 v255, v20, v21
	ds_write_b64 v251, v[254:255] offset:4608
	v_pk_add_f32 v[222:223], v[222:223], v[18:19]
	v_pk_fma_f32 v[194:195], v[18:19], v[18:19], v[194:195]
	v_pk_add_f32 v[220:221], v[220:221], v[20:21]
	v_pk_fma_f32 v[192:193], v[20:21], v[20:21], v[192:193]
	v_cvt_pk_f16_f32 v252, v22, v23
	v_cvt_pk_f16_f32 v253, v24, v25
	ds_write_b64 v251, v[252:253] offset:4624
	v_pk_add_f32 v[218:219], v[218:219], v[22:23]
	v_pk_fma_f32 v[184:185], v[22:23], v[22:23], v[184:185]
	v_pk_add_f32 v[216:217], v[216:217], v[24:25]
	v_pk_fma_f32 v[166:167], v[24:25], v[24:25], v[166:167]
	v_cvt_pk_f16_f32 v254, v26, v27
	v_cvt_pk_f16_f32 v255, v28, v29
	ds_write_b64 v251, v[254:255] offset:4640
	v_pk_add_f32 v[214:215], v[214:215], v[26:27]
	v_pk_fma_f32 v[164:165], v[26:27], v[26:27], v[164:165]
	v_pk_add_f32 v[204:205], v[204:205], v[28:29]
	v_pk_fma_f32 v[162:163], v[28:29], v[28:29], v[162:163]
	v_cvt_pk_f16_f32 v252, v30, v31
	v_cvt_pk_f16_f32 v253, v32, v33
	ds_write_b64 v251, v[252:253] offset:4656
	v_pk_add_f32 v[202:203], v[202:203], v[30:31]
	v_pk_fma_f32 v[160:161], v[30:31], v[30:31], v[160:161]
	v_pk_add_f32 v[196:197], v[196:197], v[32:33]
	v_pk_fma_f32 v[156:157], v[32:33], v[32:33], v[156:157]
	s_nop 7
	s_waitcnt lgkmcnt(0)
	s_barrier
	s_nop 1
	ds_read_b128 v[16:19], v159 offset:43520
	s_waitcnt lgkmcnt(0)
	v_mfma_f32_32x32x16_f16 v[32:47], v[16:19], v[126:129], 0
	ds_read_b128 v[2:5], v159 offset:34816
	s_waitcnt lgkmcnt(0)
	v_mfma_f32_32x32x16_f16 v[48:63], v[2:5], v[126:129], 0
	ds_read_b128 v[126:129], v159 offset:34848
	s_waitcnt lgkmcnt(0)
	v_mfma_f32_32x32x16_f16 v[48:63], v[126:129], v[118:121], v[48:63]
	v_mfma_f32_32x32x16_f16 v[0:15], v[122:125], v[2:5], v[168:183]
	v_mfma_f32_32x32x16_f16 v[0:15], v[114:117], v[126:129], v[0:15]
	v_mfma_f32_32x32x16_f16 v[16:31], v[122:125], v[16:19], v[168:183]
	ds_read_b128 v[122:125], v159 offset:43552
	s_waitcnt lgkmcnt(0)
	v_mfma_f32_32x32x16_f16 v[32:47], v[122:125], v[118:121], v[32:47]
	v_mfma_f32_32x32x16_f16 v[16:31], v[114:117], v[122:125], v[16:31]
	ds_read_b128 v[118:121], v159 offset:34880
	ds_read_b128 v[114:117], v159 offset:43584
	s_waitcnt lgkmcnt(1)
	v_mfma_f32_32x32x16_f16 v[48:63], v[118:121], v[110:113], v[48:63]
	s_waitcnt lgkmcnt(0)
	v_mfma_f32_32x32x16_f16 v[32:47], v[114:117], v[110:113], v[32:47]
	v_mfma_f32_32x32x16_f16 v[0:15], v[106:109], v[118:121], v[0:15]
	ds_read_b128 v[110:113], v159 offset:34912
	v_mfma_f32_32x32x16_f16 v[16:31], v[106:109], v[114:117], v[16:31]
	ds_read_b128 v[106:109], v159 offset:43616
	s_waitcnt lgkmcnt(1)
	v_mfma_f32_32x32x16_f16 v[48:63], v[110:113], v[102:105], v[48:63]
	s_waitcnt lgkmcnt(0)
	v_mfma_f32_32x32x16_f16 v[32:47], v[106:109], v[102:105], v[32:47]
	v_mfma_f32_32x32x16_f16 v[0:15], v[98:101], v[110:113], v[0:15]
	ds_read_b128 v[102:105], v159 offset:34944
	v_mfma_f32_32x32x16_f16 v[16:31], v[98:101], v[106:109], v[16:31]
	ds_read_b128 v[98:101], v159 offset:43648
	s_waitcnt lgkmcnt(1)
	v_mfma_f32_32x32x16_f16 v[48:63], v[102:105], v[94:97], v[48:63]
	s_waitcnt lgkmcnt(0)
	v_mfma_f32_32x32x16_f16 v[32:47], v[98:101], v[94:97], v[32:47]
	v_mfma_f32_32x32x16_f16 v[0:15], v[86:89], v[102:105], v[0:15]
	ds_read_b128 v[94:97], v159 offset:34976
	v_mfma_f32_32x32x16_f16 v[16:31], v[86:89], v[98:101], v[16:31]
	ds_read_b128 v[86:89], v159 offset:43680
	s_waitcnt lgkmcnt(1)
	v_mfma_f32_32x32x16_f16 v[48:63], v[94:97], v[90:93], v[48:63]
	s_waitcnt lgkmcnt(0)
	v_mfma_f32_32x32x16_f16 v[32:47], v[86:89], v[90:93], v[32:47]
	v_mfma_f32_32x32x16_f16 v[0:15], v[78:81], v[94:97], v[0:15]
	ds_read_b128 v[90:93], v159 offset:35008
	v_mfma_f32_32x32x16_f16 v[16:31], v[78:81], v[86:89], v[16:31]
	ds_read_b128 v[78:81], v159 offset:43712
	s_waitcnt lgkmcnt(1)
	v_mfma_f32_32x32x16_f16 v[48:63], v[90:93], v[82:85], v[48:63]
	s_waitcnt lgkmcnt(0)
	v_mfma_f32_32x32x16_f16 v[32:47], v[78:81], v[82:85], v[32:47]
	v_mfma_f32_32x32x16_f16 v[0:15], v[70:73], v[90:93], v[0:15]
	ds_read_b128 v[82:85], v159 offset:35040
	v_mfma_f32_32x32x16_f16 v[16:31], v[70:73], v[78:81], v[16:31]
	ds_read_b128 v[70:73], v159 offset:43744
	s_waitcnt lgkmcnt(1)
	v_mfma_f32_32x32x16_f16 v[48:63], v[82:85], v[74:77], v[48:63]
	v_mfma_f32_32x32x16_f16 v[0:15], v[66:69], v[82:85], v[0:15]
	s_nop 3
	s_nop 6
	v_cvt_pk_f16_f32 v55, v54, v55
	v_cvt_pk_f16_f32 v54, v52, v53
	v_cvt_pk_f16_f32 v53, v50, v51
	v_cvt_pk_f16_f32 v52, v48, v49
	s_waitcnt vmcnt(3)
	s_waitcnt lgkmcnt(0)
	v_mfma_f32_32x32x16_f16 v[16:31], v[66:69], v[70:73], v[16:31]
	v_lshrrev_b32_e32 v69, 16, v139
	v_mfma_f32_32x32x16_f16 v[32:47], v[70:73], v[74:77], v[32:47]
	v_lshrrev_b32_e32 v70, 8, v139
	v_perm_b32 v69, v70, v69, s4
	v_perm_b32 v66, v240, v138, s42
	v_perm_b32 v67, v240, v138, s43
	v_perm_b32 v68, v240, v139, s42
	v_or_b32_e32 v69, 0x64006400, v69
	v_pk_add_f16 v66, v66, s5 op_sel_hi:[1,0]
	v_pk_add_f16 v67, v67, s5 op_sel_hi:[1,0]
	v_pk_add_f16 v68, v68, s5 op_sel_hi:[1,0]
	v_pk_add_f16 v69, v69, s5 op_sel_hi:[1,0]
	s_nop 1
	v_mfma_f32_32x32x16_f16 v[0:15], v[52:55], v[66:69], v[0:15]
	v_perm_b32 v48, v240, v136, s42
	v_perm_b32 v49, v240, v136, s43
	v_perm_b32 v50, v240, v137, s42
	v_perm_b32 v51, v240, v137, s43
	v_pk_add_f16 v48, v48, s5 op_sel_hi:[1,0]
	v_pk_add_f16 v49, v49, s5 op_sel_hi:[1,0]
	v_pk_add_f16 v50, v50, s5 op_sel_hi:[1,0]
	v_pk_add_f16 v51, v51, s5 op_sel_hi:[1,0]
	v_cvt_pk_f16_f32 v39, v38, v39
	v_cvt_pk_f16_f32 v38, v36, v37
	v_mfma_f32_32x32x16_f16 v[16:31], v[52:55], v[48:51], v[16:31]
	v_perm_b32 v48, v240, v134, s42
	v_perm_b32 v49, v240, v134, s43
	v_perm_b32 v50, v240, v135, s42
	v_perm_b32 v51, v240, v135, s43
	v_pk_add_f16 v48, v48, s5 op_sel_hi:[1,0]
	v_pk_add_f16 v49, v49, s5 op_sel_hi:[1,0]
	v_pk_add_f16 v50, v50, s5 op_sel_hi:[1,0]
	v_pk_add_f16 v51, v51, s5 op_sel_hi:[1,0]
	v_cvt_pk_f16_f32 v55, v62, v63
	v_cvt_pk_f16_f32 v54, v60, v61
	v_cvt_pk_f16_f32 v53, v58, v59
	v_cvt_pk_f16_f32 v52, v56, v57
	s_waitcnt vmcnt(2)
	v_cvt_pk_f16_f32 v37, v34, v35
	v_mfma_f32_32x32x16_f16 v[0:15], v[52:55], v[48:51], v[0:15]
	v_perm_b32 v48, v240, v142, s42
	v_perm_b32 v49, v240, v142, s43
	v_perm_b32 v50, v240, v143, s42
	v_perm_b32 v51, v240, v143, s43
	v_pk_add_f16 v48, v48, s5 op_sel_hi:[1,0]
	v_pk_add_f16 v49, v49, s5 op_sel_hi:[1,0]
	v_pk_add_f16 v50, v50, s5 op_sel_hi:[1,0]
	v_pk_add_f16 v51, v51, s5 op_sel_hi:[1,0]
	v_cvt_pk_f16_f32 v36, v32, v33
	s_waitcnt vmcnt(1)
	v_mfma_f32_32x32x16_f16 v[16:31], v[52:55], v[48:51], v[16:31]
	v_lshrrev_b32_e32 v51, 16, v133
	v_lshrrev_b32_e32 v52, 8, v133
	v_perm_b32 v51, v52, v51, s4
	v_perm_b32 v48, v240, v132, s42
	v_perm_b32 v49, v240, v132, s43
	v_perm_b32 v50, v240, v133, s42
	v_or_b32_e32 v51, 0x64006400, v51
	v_pk_add_f16 v48, v48, s5 op_sel_hi:[1,0]
	v_pk_add_f16 v49, v49, s5 op_sel_hi:[1,0]
	v_pk_add_f16 v50, v50, s5 op_sel_hi:[1,0]
	v_pk_add_f16 v51, v51, s5 op_sel_hi:[1,0]
	s_nop 1
	v_mfma_f32_32x32x16_f16 v[0:15], v[36:39], v[48:51], v[0:15]
	v_perm_b32 v32, v240, v140, s42
	v_perm_b32 v33, v240, v140, s43
	v_perm_b32 v34, v240, v141, s42
	v_perm_b32 v35, v240, v141, s43
	v_pk_add_f16 v32, v32, s5 op_sel_hi:[1,0]
	v_pk_add_f16 v33, v33, s5 op_sel_hi:[1,0]
	v_pk_add_f16 v34, v34, s5 op_sel_hi:[1,0]
	v_pk_add_f16 v35, v35, s5 op_sel_hi:[1,0]
	s_nop 1
	v_mfma_f32_32x32x16_f16 v[16:31], v[36:39], v[32:35], v[16:31]
	v_perm_b32 v32, v240, v130, s42
	v_perm_b32 v33, v240, v130, s43
	v_perm_b32 v34, v240, v131, s42
	v_perm_b32 v35, v240, v131, s43
	v_pk_add_f16 v32, v32, s5 op_sel_hi:[1,0]
	v_pk_add_f16 v33, v33, s5 op_sel_hi:[1,0]
	v_pk_add_f16 v34, v34, s5 op_sel_hi:[1,0]
	v_pk_add_f16 v35, v35, s5 op_sel_hi:[1,0]
	v_cvt_pk_f16_f32 v39, v46, v47
	v_cvt_pk_f16_f32 v38, v44, v45
	v_cvt_pk_f16_f32 v37, v42, v43
	v_cvt_pk_f16_f32 v36, v40, v41
	s_waitcnt vmcnt(0)
	s_nop 0
	v_mfma_f32_32x32x16_f16 v[0:15], v[36:39], v[32:35], v[0:15]
	v_perm_b32 v32, v240, v64, s42
	v_perm_b32 v33, v240, v64, s43
	v_perm_b32 v34, v240, v65, s42
	v_perm_b32 v35, v240, v65, s43
	v_pk_add_f16 v32, v32, s5 op_sel_hi:[1,0]
	v_pk_add_f16 v33, v33, s5 op_sel_hi:[1,0]
	v_pk_add_f16 v34, v34, s5 op_sel_hi:[1,0]
	v_pk_add_f16 v35, v35, s5 op_sel_hi:[1,0]
	s_nop 3
	v_mfma_f32_32x32x16_f16 v[16:31], v[36:39], v[32:35], v[16:31]
	s_nop 7
	s_nop 4
	v_cvt_pk_f16_f32 v254, v0, v1
	v_cvt_pk_f16_f32 v255, v2, v3
	ds_write_b64 v251, v[254:255] offset:18432
	v_pk_add_f32 v[222:223], v[222:223], v[0:1]
	v_pk_fma_f32 v[194:195], v[0:1], v[0:1], v[194:195]
	v_pk_add_f32 v[220:221], v[220:221], v[2:3]
	v_pk_fma_f32 v[192:193], v[2:3], v[2:3], v[192:193]
	v_cvt_pk_f16_f32 v252, v4, v5
	v_cvt_pk_f16_f32 v253, v6, v7
	ds_write_b64 v251, v[252:253] offset:18448
	v_pk_add_f32 v[218:219], v[218:219], v[4:5]
	v_pk_fma_f32 v[184:185], v[4:5], v[4:5], v[184:185]
	v_pk_add_f32 v[216:217], v[216:217], v[6:7]
	v_pk_fma_f32 v[166:167], v[6:7], v[6:7], v[166:167]
	v_cvt_pk_f16_f32 v254, v8, v9
	v_cvt_pk_f16_f32 v255, v10, v11
	ds_write_b64 v251, v[254:255] offset:18464
	v_pk_add_f32 v[214:215], v[214:215], v[8:9]
	v_pk_fma_f32 v[164:165], v[8:9], v[8:9], v[164:165]
	v_pk_add_f32 v[204:205], v[204:205], v[10:11]
	v_pk_fma_f32 v[162:163], v[10:11], v[10:11], v[162:163]
	v_cvt_pk_f16_f32 v252, v12, v13
	v_cvt_pk_f16_f32 v253, v14, v15
	ds_write_b64 v251, v[252:253] offset:18480
	v_pk_add_f32 v[202:203], v[202:203], v[12:13]
	v_pk_fma_f32 v[160:161], v[12:13], v[12:13], v[160:161]
	v_pk_add_f32 v[196:197], v[196:197], v[14:15]
	v_pk_fma_f32 v[156:157], v[14:15], v[14:15], v[156:157]
	v_cvt_pk_f16_f32 v254, v16, v17
	v_cvt_pk_f16_f32 v255, v18, v19
	ds_write_b64 v251, v[254:255] offset:23040
	v_pk_add_f32 v[222:223], v[222:223], v[16:17]
	v_pk_fma_f32 v[194:195], v[16:17], v[16:17], v[194:195]
	v_pk_add_f32 v[220:221], v[220:221], v[18:19]
	v_pk_fma_f32 v[192:193], v[18:19], v[18:19], v[192:193]
	v_cvt_pk_f16_f32 v252, v20, v21
	v_cvt_pk_f16_f32 v253, v22, v23
	ds_write_b64 v251, v[252:253] offset:23056
	v_pk_add_f32 v[218:219], v[218:219], v[20:21]
	v_pk_fma_f32 v[184:185], v[20:21], v[20:21], v[184:185]
	v_pk_add_f32 v[216:217], v[216:217], v[22:23]
	v_pk_fma_f32 v[166:167], v[22:23], v[22:23], v[166:167]
	v_cvt_pk_f16_f32 v254, v24, v25
	v_cvt_pk_f16_f32 v255, v26, v27
	ds_write_b64 v251, v[254:255] offset:23072
	v_pk_add_f32 v[214:215], v[214:215], v[24:25]
	v_pk_fma_f32 v[164:165], v[24:25], v[24:25], v[164:165]
	v_pk_add_f32 v[204:205], v[204:205], v[26:27]
	v_pk_fma_f32 v[162:163], v[26:27], v[26:27], v[162:163]
	v_cvt_pk_f16_f32 v252, v28, v29
	v_cvt_pk_f16_f32 v253, v30, v31
	ds_write_b64 v251, v[252:253] offset:23088
	v_pk_add_f32 v[202:203], v[202:203], v[28:29]
	v_pk_fma_f32 v[160:161], v[28:29], v[28:29], v[160:161]
	v_pk_add_f32 v[196:197], v[196:197], v[30:31]
	v_pk_fma_f32 v[156:157], v[30:31], v[30:31], v[156:157]
	s_nop 4
	s_nop 0
	v_add_f32_dpp v222, v222, v222 row_half_mirror row_mask:0xf bank_mask:0x5
	v_add_f32_dpp v222, v223, v223 row_half_mirror row_mask:0xf bank_mask:0xa
	v_add_f32_dpp v220, v220, v220 row_half_mirror row_mask:0xf bank_mask:0x5
	v_add_f32_dpp v220, v221, v221 row_half_mirror row_mask:0xf bank_mask:0xa
	v_add_f32_dpp v218, v218, v218 row_half_mirror row_mask:0xf bank_mask:0x5
	v_add_f32_dpp v218, v219, v219 row_half_mirror row_mask:0xf bank_mask:0xa
	v_add_f32_dpp v216, v216, v216 row_half_mirror row_mask:0xf bank_mask:0x5
	v_add_f32_dpp v216, v217, v217 row_half_mirror row_mask:0xf bank_mask:0xa
	v_add_f32_dpp v214, v214, v214 row_half_mirror row_mask:0xf bank_mask:0x5
	v_add_f32_dpp v214, v215, v215 row_half_mirror row_mask:0xf bank_mask:0xa
	v_add_f32_dpp v204, v204, v204 row_half_mirror row_mask:0xf bank_mask:0x5
	v_add_f32_dpp v204, v205, v205 row_half_mirror row_mask:0xf bank_mask:0xa
	v_add_f32_dpp v202, v202, v202 row_half_mirror row_mask:0xf bank_mask:0x5
	v_add_f32_dpp v202, v203, v203 row_half_mirror row_mask:0xf bank_mask:0xa
	v_add_f32_dpp v196, v196, v196 row_half_mirror row_mask:0xf bank_mask:0x5
	v_add_f32_dpp v196, v197, v197 row_half_mirror row_mask:0xf bank_mask:0xa
	v_add_f32_dpp v194, v194, v194 row_half_mirror row_mask:0xf bank_mask:0x5
	v_add_f32_dpp v194, v195, v195 row_half_mirror row_mask:0xf bank_mask:0xa
	v_add_f32_dpp v192, v192, v192 row_half_mirror row_mask:0xf bank_mask:0x5
	v_add_f32_dpp v192, v193, v193 row_half_mirror row_mask:0xf bank_mask:0xa
	v_add_f32_dpp v184, v184, v184 row_half_mirror row_mask:0xf bank_mask:0x5
	v_add_f32_dpp v184, v185, v185 row_half_mirror row_mask:0xf bank_mask:0xa
	v_add_f32_dpp v166, v166, v166 row_half_mirror row_mask:0xf bank_mask:0x5
	v_add_f32_dpp v166, v167, v167 row_half_mirror row_mask:0xf bank_mask:0xa
	v_add_f32_dpp v164, v164, v164 row_half_mirror row_mask:0xf bank_mask:0x5
	v_add_f32_dpp v164, v165, v165 row_half_mirror row_mask:0xf bank_mask:0xa
	v_add_f32_dpp v162, v162, v162 row_half_mirror row_mask:0xf bank_mask:0x5
	v_add_f32_dpp v162, v163, v163 row_half_mirror row_mask:0xf bank_mask:0xa
	v_add_f32_dpp v160, v160, v160 row_half_mirror row_mask:0xf bank_mask:0x5
	v_add_f32_dpp v160, v161, v161 row_half_mirror row_mask:0xf bank_mask:0xa
	v_add_f32_dpp v156, v156, v156 row_half_mirror row_mask:0xf bank_mask:0x5
	v_add_f32_dpp v156, v157, v157 row_half_mirror row_mask:0xf bank_mask:0xa
	v_add_f32_dpp v222, v222, v222 row_ror:8 row_mask:0xf bank_mask:0x3
	v_add_f32_dpp v222, v220, v220 row_ror:8 row_mask:0xf bank_mask:0xc
	v_add_f32_dpp v218, v218, v218 row_ror:8 row_mask:0xf bank_mask:0x3
	v_add_f32_dpp v218, v216, v216 row_ror:8 row_mask:0xf bank_mask:0xc
	v_add_f32_dpp v214, v214, v214 row_ror:8 row_mask:0xf bank_mask:0x3
	v_add_f32_dpp v214, v204, v204 row_ror:8 row_mask:0xf bank_mask:0xc
	v_add_f32_dpp v202, v202, v202 row_ror:8 row_mask:0xf bank_mask:0x3
	v_add_f32_dpp v202, v196, v196 row_ror:8 row_mask:0xf bank_mask:0xc
	v_add_f32_dpp v194, v194, v194 row_ror:8 row_mask:0xf bank_mask:0x3
	v_add_f32_dpp v194, v192, v192 row_ror:8 row_mask:0xf bank_mask:0xc
	v_add_f32_dpp v184, v184, v184 row_ror:8 row_mask:0xf bank_mask:0x3
	v_add_f32_dpp v184, v166, v166 row_ror:8 row_mask:0xf bank_mask:0xc
	v_add_f32_dpp v164, v164, v164 row_ror:8 row_mask:0xf bank_mask:0x3
	v_add_f32_dpp v164, v162, v162 row_ror:8 row_mask:0xf bank_mask:0xc
	v_add_f32_dpp v160, v160, v160 row_ror:8 row_mask:0xf bank_mask:0x3
	v_add_f32_dpp v160, v156, v156 row_ror:8 row_mask:0xf bank_mask:0xc
	v_add_f32_dpp v222, v222, v222 quad_perm:[1,0,3,2] row_mask:0xf bank_mask:0xf
	v_add_f32_dpp v218, v218, v218 quad_perm:[1,0,3,2] row_mask:0xf bank_mask:0xf
	v_add_f32_dpp v214, v214, v214 quad_perm:[1,0,3,2] row_mask:0xf bank_mask:0xf
	v_add_f32_dpp v202, v202, v202 quad_perm:[1,0,3,2] row_mask:0xf bank_mask:0xf
	v_add_f32_dpp v194, v194, v194 quad_perm:[1,0,3,2] row_mask:0xf bank_mask:0xf
	v_add_f32_dpp v184, v184, v184 quad_perm:[1,0,3,2] row_mask:0xf bank_mask:0xf
	v_add_f32_dpp v164, v164, v164 quad_perm:[1,0,3,2] row_mask:0xf bank_mask:0xf
	v_add_f32_dpp v160, v160, v160 quad_perm:[1,0,3,2] row_mask:0xf bank_mask:0xf
	v_add_f32_dpp v222, v222, v222 quad_perm:[2,3,0,1] row_mask:0xf bank_mask:0xf
	v_add_f32_dpp v218, v218, v218 quad_perm:[2,3,0,1] row_mask:0xf bank_mask:0xf
	v_add_f32_dpp v214, v214, v214 quad_perm:[2,3,0,1] row_mask:0xf bank_mask:0xf
	v_add_f32_dpp v202, v202, v202 quad_perm:[2,3,0,1] row_mask:0xf bank_mask:0xf
	v_add_f32_dpp v194, v194, v194 quad_perm:[2,3,0,1] row_mask:0xf bank_mask:0xf
	v_add_f32_dpp v184, v184, v184 quad_perm:[2,3,0,1] row_mask:0xf bank_mask:0xf
	v_add_f32_dpp v164, v164, v164 quad_perm:[2,3,0,1] row_mask:0xf bank_mask:0xf
	v_add_f32_dpp v160, v160, v160 quad_perm:[2,3,0,1] row_mask:0xf bank_mask:0xf
	s_mov_b32 exec_lo, 0x11111111
	s_mov_b32 exec_hi, 0x11111111
	ds_add_f32 v250, v222 offset:0
	ds_add_f32 v250, v218 offset:32
	ds_add_f32 v250, v214 offset:64
	ds_add_f32 v250, v202 offset:96
	ds_add_f32 v250, v194 offset:256
	ds_add_f32 v250, v184 offset:288
	ds_add_f32 v250, v164 offset:320
	ds_add_f32 v250, v160 offset:352
	s_mov_b64 exec, -1
	s_waitcnt lgkmcnt(0)
	s_barrier
	s_cmp_lg_u32 s50, 0
	s_cbranch_scc1 .LBB2_27
	v_mbcnt_lo_u32_b32 v2, -1, 0
	v_mbcnt_hi_u32_b32 v2, -1, v2
	v_and_b32_e32 v3, 32, v2
	v_add_u32_e32 v4, v2, v3
	v_lshl_add_u32 v5, v4, 2, s49
	ds_read_b32 v6, v5
	v_lshl_add_u32 v4, v3, 1, v4
	v_add_u32_e32 v4, s48, v4
	v_lshlrev_b32_e32 v4, 2, v4
	s_waitcnt lgkmcnt(0)
	global_atomic_add_f32 v4, v6, s[46:47]

.LBB3_24:
	s_or_b64 exec, exec, s[2:3]
	v_and_b32_e32 v1, 31, v0
	v_lshlrev_b32_e32 v2, 2, v1
	v_lshl_or_b32 v2, s13, 7, v2
	v_or_b32_e32 v2, 0x1ee00, v2
	v_lshrrev_b32_e32 v158, 5, v156
	s_waitcnt lgkmcnt(0)
	s_barrier
	v_lshlrev_b32_e32 v250, 4, v158
	v_lshl_or_b32 v250, s13, 7, v250
	v_or_b32_e32 v254, 0x1ee00, v250
	ds_read_b128 v[168:171], v254 offset:0
	ds_read_b128 v[172:175], v254 offset:32
	ds_read_b128 v[176:179], v254 offset:64
	ds_read_b128 v[180:183], v254 offset:96
	v_bfe_u32 v255, v156, 2, 2
	v_lshl_add_u32 v250, v255, 2, v250
	v_add_u32_e32 v250, 0x1e400, v250
	s_waitcnt lgkmcnt(0)
	s_barrier
	ds_read_b32 v157, v2
	v_mul_u32_u24_e32 v2, 0x88, v1
	s_mul_i32 s0, s16, 0x4400
	v_lshlrev_b32_e32 v2, 1, v2
	v_lshlrev_b32_e32 v3, 4, v158
	v_mov_b32_e32 v138, v0
	v_add3_u32 v159, s0, v2, v3
	ds_read_b128 v[2:5], v159
	ds_read_b128 v[18:21], v159 offset:8704
	ds_read_b128 v[130:133], v159 offset:32
	s_waitcnt vmcnt(10) lgkmcnt(2)
	v_mfma_f32_32x32x16_f16 v[50:65], v[2:5], v[126:129], 0
	s_mov_b32 s2, 0xc060c00
	s_mov_b32 s3, 0xe400
	s_mulk_i32 s16, 0x2400
	s_lshl_b32 s0, s13, 6
	s_or_b32 s0, s16, s0
	s_add_i32 s0, s0, 0x11000
	v_mul_u32_u24_e32 v251, 0x90, v1
	v_lshl_add_u32 v251, v158, 3, v251
	v_add_u32_e32 v251, s0, v251
	s_waitcnt lgkmcnt(1)
	v_mfma_f32_32x32x16_f16 v[34:49], v[18:21], v[126:129], 0
	s_or_b32 s0, s10, 2
	s_ashr_i32 s1, s0, 31
	s_lshl_b64 s[0:1], s[0:1], 12
	s_add_u32 s0, s8, s0
	s_addc_u32 s1, s9, s1
	v_cmp_gt_u32_e32 vcc, 32, v156
	v_mfma_f32_32x32x16_f16 v[2:17], v[122:125], v[2:5], v[168:183]
	v_mfma_f32_32x32x16_f16 v[18:33], v[122:125], v[18:21], v[168:183]
	ds_read_b128 v[134:137], v159 offset:8736
	ds_read_b128 v[160:163], v159 offset:64
	s_waitcnt vmcnt(8) lgkmcnt(2)
	v_mfma_f32_32x32x16_f16 v[50:65], v[130:133], v[118:121], v[50:65]
	s_waitcnt lgkmcnt(1)
	v_mfma_f32_32x32x16_f16 v[34:49], v[134:137], v[118:121], v[34:49]
	v_mfma_f32_32x32x16_f16 v[2:17], v[114:117], v[130:133], v[2:17]
	v_mfma_f32_32x32x16_f16 v[18:33], v[114:117], v[134:137], v[18:33]
	ds_read_b128 v[130:133], v159 offset:8768
	ds_read_b128 v[134:137], v159 offset:96
	s_waitcnt vmcnt(6) lgkmcnt(2)
	v_mfma_f32_32x32x16_f16 v[50:65], v[160:163], v[110:113], v[50:65]
	s_waitcnt lgkmcnt(1)
	v_mfma_f32_32x32x16_f16 v[34:49], v[130:133], v[110:113], v[34:49]
	v_mfma_f32_32x32x16_f16 v[2:17], v[106:109], v[160:163], v[2:17]
	v_mfma_f32_32x32x16_f16 v[18:33], v[106:109], v[130:133], v[18:33]
	ds_read_b128 v[130:133], v159 offset:8800
	ds_read_b128 v[160:163], v159 offset:128
	s_waitcnt vmcnt(4) lgkmcnt(2)
	v_mfma_f32_32x32x16_f16 v[50:65], v[134:137], v[102:105], v[50:65]
	s_waitcnt lgkmcnt(1)
	v_mfma_f32_32x32x16_f16 v[34:49], v[130:133], v[102:105], v[34:49]
	v_mfma_f32_32x32x16_f16 v[2:17], v[98:101], v[134:137], v[2:17]
	v_mfma_f32_32x32x16_f16 v[18:33], v[98:101], v[130:133], v[18:33]
	ds_read_b128 v[130:133], v159 offset:8832
	ds_read_b128 v[134:137], v159 offset:160
	s_waitcnt vmcnt(3) lgkmcnt(2)
	v_mfma_f32_32x32x16_f16 v[50:65], v[160:163], v[94:97], v[50:65]
	s_waitcnt lgkmcnt(1)
	v_mfma_f32_32x32x16_f16 v[34:49], v[130:133], v[94:97], v[34:49]
	v_mfma_f32_32x32x16_f16 v[2:17], v[86:89], v[160:163], v[2:17]
	v_mfma_f32_32x32x16_f16 v[18:33], v[86:89], v[130:133], v[18:33]
	ds_read_b128 v[130:133], v159 offset:8864
	ds_read_b128 v[160:163], v159 offset:192
	s_waitcnt vmcnt(2) lgkmcnt(2)
	v_mfma_f32_32x32x16_f16 v[50:65], v[134:137], v[90:93], v[50:65]
	s_waitcnt lgkmcnt(1)
	v_mfma_f32_32x32x16_f16 v[34:49], v[130:133], v[90:93], v[34:49]
	v_mfma_f32_32x32x16_f16 v[2:17], v[78:81], v[134:137], v[2:17]
	v_mfma_f32_32x32x16_f16 v[18:33], v[78:81], v[130:133], v[18:33]
	ds_read_b128 v[130:133], v159 offset:8896
	ds_read_b128 v[164:167], v159 offset:224
	s_waitcnt vmcnt(1) lgkmcnt(2)
	v_mfma_f32_32x32x16_f16 v[50:65], v[160:163], v[82:85], v[50:65]
	s_waitcnt lgkmcnt(1)
	v_mfma_f32_32x32x16_f16 v[34:49], v[130:133], v[82:85], v[34:49]
	v_mfma_f32_32x32x16_f16 v[2:17], v[70:73], v[160:163], v[2:17]
	v_mfma_f32_32x32x16_f16 v[18:33], v[70:73], v[130:133], v[18:33]
	v_lshlrev_b32_e32 v130, 3, v138
	v_and_b32_e32 v241, 0x1f8, v130
	global_load_dwordx2 v[138:139], v241, s[0:1]
	global_load_dwordx2 v[134:135], v241, s[0:1] offset:512
	global_load_dwordx2 v[132:133], v241, s[0:1] offset:1024
	global_load_dwordx2 v[130:131], v241, s[0:1] offset:1536
	global_load_dwordx2 v[136:137], v241, s[0:1] offset:2048
	s_waitcnt vmcnt(5) lgkmcnt(0)
	v_mfma_f32_32x32x16_f16 v[50:65], v[164:167], v[74:77], v[50:65]
	v_mfma_f32_32x32x16_f16 v[2:17], v[66:69], v[164:167], v[2:17]
	s_nop 10
	v_cvt_pk_f16_f32 v57, v56, v57
	v_cvt_pk_f16_f32 v56, v54, v55
	v_cvt_pk_f16_f32 v55, v52, v53
	v_cvt_pk_f16_f32 v54, v50, v51
	v_perm_b32 v50, v240, v154, s42
	v_perm_b32 v51, v240, v154, s43
	v_perm_b32 v52, v240, v155, s42
	v_perm_b32 v53, v240, v155, s43
	v_pk_add_f16 v50, v50, s3 op_sel_hi:[1,0]
	v_pk_add_f16 v51, v51, s3 op_sel_hi:[1,0]
	v_pk_add_f16 v52, v52, s3 op_sel_hi:[1,0]
	v_pk_add_f16 v53, v53, s3 op_sel_hi:[1,0]
	v_cvt_pk_f16_f32 v65, v64, v65
	v_cvt_pk_f16_f32 v64, v62, v63
	v_cvt_pk_f16_f32 v63, v60, v61
	v_cvt_pk_f16_f32 v62, v58, v59
	v_mfma_f32_32x32x16_f16 v[2:17], v[54:57], v[50:53], v[2:17]
	v_perm_b32 v58, v240, v150, s42
	v_perm_b32 v59, v240, v150, s43
	v_perm_b32 v60, v240, v151, s42
	v_perm_b32 v61, v240, v151, s43
	v_pk_add_f16 v58, v58, s3 op_sel_hi:[1,0]
	v_pk_add_f16 v59, v59, s3 op_sel_hi:[1,0]
	v_pk_add_f16 v60, v60, s3 op_sel_hi:[1,0]
	v_pk_add_f16 v61, v61, s3 op_sel_hi:[1,0]
	s_nop 1
	v_mfma_f32_32x32x16_f16 v[2:17], v[62:65], v[58:61], v[2:17]
	ds_read_b128 v[160:163], v159 offset:8928
	v_perm_b32 v155, v240, v152, s43
	v_perm_b32 v164, v240, v153, s42
	s_waitcnt lgkmcnt(0)
	v_mfma_f32_32x32x16_f16 v[18:33], v[66:69], v[160:163], v[18:33]
	v_perm_b32 v154, v240, v152, s42
	v_perm_b32 v165, v240, v153, s43
	v_pk_add_f16 v152, v154, s3 op_sel_hi:[1,0]
	v_pk_add_f16 v153, v155, s3 op_sel_hi:[1,0]
	v_pk_add_f16 v154, v164, s3 op_sel_hi:[1,0]
	v_pk_add_f16 v155, v165, s3 op_sel_hi:[1,0]
	v_mfma_f32_32x32x16_f16 v[34:49], v[160:163], v[74:77], v[34:49]
	v_perm_b32 v151, v240, v148, s43
	v_perm_b32 v164, v240, v149, s42
	v_mfma_f32_32x32x16_f16 v[18:33], v[54:57], v[152:155], v[18:33]
	v_perm_b32 v150, v240, v148, s42
	v_perm_b32 v165, v240, v149, s43
	v_pk_add_f16 v148, v150, s3 op_sel_hi:[1,0]
	v_pk_add_f16 v149, v151, s3 op_sel_hi:[1,0]
	v_pk_add_f16 v150, v164, s3 op_sel_hi:[1,0]
	v_pk_add_f16 v151, v165, s3 op_sel_hi:[1,0]
	s_nop 2
	v_cvt_pk_f16_f32 v41, v40, v41
	v_cvt_pk_f16_f32 v40, v38, v39
	v_cvt_pk_f16_f32 v38, v34, v35
	v_cvt_pk_f16_f32 v39, v36, v37
	v_mfma_f32_32x32x16_f16 v[18:33], v[62:65], v[148:151], v[18:33]
	v_perm_b32 v34, v240, v146, s42
	v_perm_b32 v35, v240, v146, s43
	v_perm_b32 v36, v240, v147, s42
	v_perm_b32 v37, v240, v147, s43
	v_pk_add_f16 v34, v34, s3 op_sel_hi:[1,0]
	v_pk_add_f16 v35, v35, s3 op_sel_hi:[1,0]
	v_pk_add_f16 v36, v36, s3 op_sel_hi:[1,0]
	v_pk_add_f16 v37, v37, s3 op_sel_hi:[1,0]
	v_perm_b32 v146, v240, v144, s42
	v_perm_b32 v144, v240, v144, s43
	v_perm_b32 v147, v240, v145, s42
	v_perm_b32 v53, v240, v145, s43
	v_pk_add_f16 v50, v146, s3 op_sel_hi:[1,0]
	v_pk_add_f16 v51, v144, s3 op_sel_hi:[1,0]
	v_pk_add_f16 v52, v147, s3 op_sel_hi:[1,0]
	v_pk_add_f16 v53, v53, s3 op_sel_hi:[1,0]
	v_cvt_pk_f16_f32 v49, v48, v49
	v_cvt_pk_f16_f32 v48, v46, v47
	v_cvt_pk_f16_f32 v47, v44, v45
	v_mfma_f32_32x32x16_f16 v[2:17], v[38:41], v[34:37], v[2:17]
	v_cvt_pk_f16_f32 v46, v42, v43
	v_mfma_f32_32x32x16_f16 v[18:33], v[38:41], v[50:53], v[18:33]
	v_perm_b32 v34, v240, v140, s42
	v_perm_b32 v35, v240, v140, s43
	v_perm_b32 v36, v240, v141, s42
	v_perm_b32 v37, v240, v141, s43
	v_perm_b32 v42, v240, v142, s42
	v_perm_b32 v43, v240, v142, s43
	v_perm_b32 v44, v240, v143, s42
	v_perm_b32 v45, v240, v143, s43
	v_pk_add_f16 v34, v34, s3 op_sel_hi:[1,0]
	v_pk_add_f16 v35, v35, s3 op_sel_hi:[1,0]
	v_pk_add_f16 v36, v36, s3 op_sel_hi:[1,0]
	v_pk_add_f16 v37, v37, s3 op_sel_hi:[1,0]
	v_pk_add_f16 v42, v42, s3 op_sel_hi:[1,0]
	v_pk_add_f16 v43, v43, s3 op_sel_hi:[1,0]
	v_pk_add_f16 v44, v44, s3 op_sel_hi:[1,0]
	v_pk_add_f16 v45, v45, s3 op_sel_hi:[1,0]
	v_mfma_f32_32x32x16_f16 v[18:33], v[46:49], v[34:37], v[18:33]
	global_load_dwordx2 v[154:155], v241, s[0:1] offset:2560
	global_load_dwordx2 v[152:153], v241, s[0:1] offset:3072
	global_load_dwordx2 v[150:151], v241, s[0:1] offset:3584
	v_mov_b32_e32 v148, v0
	s_or_b32 s0, s10, 4
	s_ashr_i32 s1, s0, 31
	s_lshl_b64 s[0:1], s[0:1], 12
	v_mfma_f32_32x32x16_f16 v[2:17], v[46:49], v[42:45], v[2:17]
	s_nop 7
	s_nop 4
	v_cvt_pk_f16_f32 v254, v2, v3
	v_cvt_pk_f16_f32 v255, v4, v5
	ds_write_b64 v251, v[254:255] offset:0
	v_cvt_pk_f16_f32 v252, v6, v7
	v_cvt_pk_f16_f32 v253, v8, v9
	ds_write_b64 v251, v[252:253] offset:16
	v_cvt_pk_f16_f32 v254, v10, v11
	v_cvt_pk_f16_f32 v255, v12, v13
	ds_write_b64 v251, v[254:255] offset:32
	v_cvt_pk_f16_f32 v252, v14, v15
	v_cvt_pk_f16_f32 v253, v16, v17
	ds_write_b64 v251, v[252:253] offset:48
	v_cvt_pk_f16_f32 v254, v18, v19
	v_cvt_pk_f16_f32 v255, v20, v21
	ds_write_b64 v251, v[254:255] offset:4608
	v_pk_add_f32 v[222:223], v[2:3], v[18:19]
	v_pk_mul_f32 v[194:195], v[2:3], v[2:3]
	v_pk_fma_f32 v[194:195], v[18:19], v[18:19], v[194:195]
	v_pk_add_f32 v[220:221], v[4:5], v[20:21]
	v_pk_mul_f32 v[192:193], v[4:5], v[4:5]
	v_pk_fma_f32 v[192:193], v[20:21], v[20:21], v[192:193]
	v_cvt_pk_f16_f32 v252, v22, v23
	v_cvt_pk_f16_f32 v253, v24, v25
	ds_write_b64 v251, v[252:253] offset:4624
	v_pk_add_f32 v[218:219], v[6:7], v[22:23]
	v_pk_mul_f32 v[184:185], v[6:7], v[6:7]
	v_pk_fma_f32 v[184:185], v[22:23], v[22:23], v[184:185]
	v_pk_add_f32 v[216:217], v[8:9], v[24:25]
	v_pk_mul_f32 v[166:167], v[8:9], v[8:9]
	v_pk_fma_f32 v[166:167], v[24:25], v[24:25], v[166:167]
	v_cvt_pk_f16_f32 v254, v26, v27
	v_cvt_pk_f16_f32 v255, v28, v29
	ds_write_b64 v251, v[254:255] offset:4640
	v_pk_add_f32 v[214:215], v[10:11], v[26:27]
	v_pk_mul_f32 v[164:165], v[10:11], v[10:11]
	v_pk_fma_f32 v[164:165], v[26:27], v[26:27], v[164:165]
	v_pk_add_f32 v[204:205], v[12:13], v[28:29]
	v_pk_mul_f32 v[162:163], v[12:13], v[12:13]
	v_pk_fma_f32 v[162:163], v[28:29], v[28:29], v[162:163]
	v_cvt_pk_f16_f32 v252, v30, v31
	v_cvt_pk_f16_f32 v253, v32, v33
	ds_write_b64 v251, v[252:253] offset:4656
	v_pk_add_f32 v[202:203], v[14:15], v[30:31]
	v_pk_mul_f32 v[160:161], v[14:15], v[14:15]
	v_pk_fma_f32 v[160:161], v[30:31], v[30:31], v[160:161]
	v_pk_add_f32 v[196:197], v[16:17], v[32:33]
	v_pk_mul_f32 v[156:157], v[16:17], v[16:17]
	v_pk_fma_f32 v[156:157], v[32:33], v[32:33], v[156:157]
	s_nop 3
	s_nop 0
	s_waitcnt lgkmcnt(0)
	s_barrier
	s_nop 4
	ds_read_b128 v[2:5], v159 offset:34816
	ds_read_b128 v[18:21], v159 offset:43520
	ds_read_b128 v[140:143], v159 offset:34848
	ds_read_b128 v[144:147], v159 offset:43552
	s_waitcnt lgkmcnt(3)
	v_mfma_f32_32x32x16_f16 v[50:65], v[2:5], v[126:129], 0
	s_add_u32 s0, s8, s0
	s_addc_u32 s1, s9, s1
	s_waitcnt lgkmcnt(2)
	v_mfma_f32_32x32x16_f16 v[34:49], v[18:21], v[126:129], 0
	v_mfma_f32_32x32x16_f16 v[2:17], v[122:125], v[2:5], v[168:183]
	v_mfma_f32_32x32x16_f16 v[18:33], v[122:125], v[18:21], v[168:183]
	ds_read_b128 v[242:245], v159 offset:34880
	ds_read_b128 v[246:249], v159 offset:43584
	s_waitcnt lgkmcnt(3)
	v_mfma_f32_32x32x16_f16 v[50:65], v[140:143], v[118:121], v[50:65]
	s_waitcnt lgkmcnt(2)
	v_mfma_f32_32x32x16_f16 v[34:49], v[144:147], v[118:121], v[34:49]
	v_mfma_f32_32x32x16_f16 v[2:17], v[114:117], v[140:143], v[2:17]
	v_mfma_f32_32x32x16_f16 v[18:33], v[114:117], v[144:147], v[18:33]
	ds_read_b128 v[140:143], v159 offset:34912
	ds_read_b128 v[144:147], v159 offset:43616
	s_waitcnt lgkmcnt(3)
	v_mfma_f32_32x32x16_f16 v[50:65], v[242:245], v[110:113], v[50:65]
	s_waitcnt lgkmcnt(2)
	v_mfma_f32_32x32x16_f16 v[34:49], v[246:249], v[110:113], v[34:49]
	v_mfma_f32_32x32x16_f16 v[2:17], v[106:109], v[242:245], v[2:17]
	v_mfma_f32_32x32x16_f16 v[18:33], v[106:109], v[246:249], v[18:33]
	ds_read_b128 v[242:245], v159 offset:34944
	ds_read_b128 v[246:249], v159 offset:43648
	s_waitcnt lgkmcnt(3)
	v_mfma_f32_32x32x16_f16 v[50:65], v[140:143], v[102:105], v[50:65]
	s_waitcnt lgkmcnt(2)
	v_mfma_f32_32x32x16_f16 v[34:49], v[144:147], v[102:105], v[34:49]
	v_mfma_f32_32x32x16_f16 v[2:17], v[98:101], v[140:143], v[2:17]
	v_mfma_f32_32x32x16_f16 v[18:33], v[98:101], v[144:147], v[18:33]
	ds_read_b128 v[186:189], v159 offset:34976
	ds_read_b128 v[206:209], v159 offset:43680
	s_waitcnt lgkmcnt(3)
	v_mfma_f32_32x32x16_f16 v[50:65], v[242:245], v[94:97], v[50:65]
	s_waitcnt lgkmcnt(2)
	v_mfma_f32_32x32x16_f16 v[34:49], v[246:249], v[94:97], v[34:49]
	v_mfma_f32_32x32x16_f16 v[2:17], v[86:89], v[242:245], v[2:17]
	v_mfma_f32_32x32x16_f16 v[18:33], v[86:89], v[246:249], v[18:33]
	ds_read_b128 v[140:143], v159 offset:35008
	ds_read_b128 v[144:147], v159 offset:43712
	s_waitcnt lgkmcnt(3)
	v_mfma_f32_32x32x16_f16 v[50:65], v[186:189], v[90:93], v[50:65]
	s_waitcnt lgkmcnt(2)
	v_mfma_f32_32x32x16_f16 v[34:49], v[206:209], v[90:93], v[34:49]
	v_mfma_f32_32x32x16_f16 v[2:17], v[78:81], v[186:189], v[2:17]
	v_mfma_f32_32x32x16_f16 v[18:33], v[78:81], v[206:209], v[18:33]
	ds_read_b128 v[186:189], v159 offset:35040
	ds_read_b128 v[206:209], v159 offset:43744
	s_waitcnt lgkmcnt(3)
	v_mfma_f32_32x32x16_f16 v[50:65], v[140:143], v[82:85], v[50:65]
	s_waitcnt lgkmcnt(2)
	v_mfma_f32_32x32x16_f16 v[34:49], v[144:147], v[82:85], v[34:49]
	v_mfma_f32_32x32x16_f16 v[2:17], v[70:73], v[140:143], v[2:17]
	v_lshlrev_b32_e32 v140, 3, v148
	v_and_b32_e32 v199, 0x1f8, v140
	global_load_dwordx2 v[148:149], v199, s[0:1]
	global_load_dwordx2 v[142:143], v199, s[0:1] offset:1024
	global_load_dwordx2 v[140:141], v199, s[0:1] offset:1536
	v_mfma_f32_32x32x16_f16 v[18:33], v[70:73], v[144:147], v[18:33]
	global_load_dwordx2 v[144:145], v199, s[0:1] offset:512
	global_load_dwordx2 v[146:147], v199, s[0:1] offset:2048
	s_waitcnt lgkmcnt(1)
	v_mfma_f32_32x32x16_f16 v[50:65], v[186:189], v[74:77], v[50:65]
	v_mfma_f32_32x32x16_f16 v[2:17], v[66:69], v[186:189], v[2:17]
	s_nop 10
	v_cvt_pk_f16_f32 v57, v56, v57
	v_cvt_pk_f16_f32 v56, v54, v55
	v_cvt_pk_f16_f32 v54, v50, v51
	s_waitcnt vmcnt(12)
	v_cvt_pk_f16_f32 v55, v52, v53
	s_waitcnt vmcnt(8)
	v_perm_b32 v50, v240, v138, s42
	v_perm_b32 v51, v240, v138, s43
	v_perm_b32 v52, v240, v139, s42
	v_perm_b32 v53, v240, v139, s43
	v_perm_b32 v139, v240, v136, s43
	v_pk_add_f16 v50, v50, s3 op_sel_hi:[1,0]
	v_pk_add_f16 v51, v51, s3 op_sel_hi:[1,0]
	v_pk_add_f16 v52, v52, s3 op_sel_hi:[1,0]
	v_pk_add_f16 v53, v53, s3 op_sel_hi:[1,0]
	v_perm_b32 v190, v240, v137, s42
	s_waitcnt lgkmcnt(0)
	v_mfma_f32_32x32x16_f16 v[18:33], v[66:69], v[206:209], v[18:33]
	v_perm_b32 v138, v240, v136, s42
	v_perm_b32 v191, v240, v137, s43
	v_pk_add_f16 v136, v138, s3 op_sel_hi:[1,0]
	v_pk_add_f16 v137, v139, s3 op_sel_hi:[1,0]
	v_pk_add_f16 v138, v190, s3 op_sel_hi:[1,0]
	v_pk_add_f16 v139, v191, s3 op_sel_hi:[1,0]
	v_cvt_pk_f16_f32 v65, v64, v65
	v_cvt_pk_f16_f32 v64, v62, v63
	v_cvt_pk_f16_f32 v63, v60, v61
	v_cvt_pk_f16_f32 v62, v58, v59
	v_mfma_f32_32x32x16_f16 v[34:49], v[206:209], v[74:77], v[34:49]
	v_mfma_f32_32x32x16_f16 v[2:17], v[54:57], v[50:53], v[2:17]
	s_waitcnt vmcnt(7)
	v_perm_b32 v58, v240, v134, s42
	v_perm_b32 v59, v240, v134, s43
	v_perm_b32 v60, v240, v135, s42
	v_perm_b32 v61, v240, v135, s43
	v_pk_add_f16 v58, v58, s3 op_sel_hi:[1,0]
	v_pk_add_f16 v59, v59, s3 op_sel_hi:[1,0]
	v_pk_add_f16 v60, v60, s3 op_sel_hi:[1,0]
	v_pk_add_f16 v61, v61, s3 op_sel_hi:[1,0]
	v_mfma_f32_32x32x16_f16 v[18:33], v[54:57], v[136:139], v[18:33]
	v_perm_b32 v134, v240, v154, s42
	v_perm_b32 v135, v240, v154, s43
	v_perm_b32 v154, v240, v155, s42
	v_perm_b32 v155, v240, v155, s43
	v_pk_add_f16 v210, v134, s3 op_sel_hi:[1,0]
	v_pk_add_f16 v211, v135, s3 op_sel_hi:[1,0]
	v_pk_add_f16 v212, v154, s3 op_sel_hi:[1,0]
	v_pk_add_f16 v213, v155, s3 op_sel_hi:[1,0]
	v_cvt_pk_f16_f32 v41, v40, v41
	v_cvt_pk_f16_f32 v40, v38, v39
	v_cvt_pk_f16_f32 v39, v36, v37
	v_cvt_pk_f16_f32 v38, v34, v35
	v_mfma_f32_32x32x16_f16 v[2:17], v[62:65], v[58:61], v[2:17]
	v_perm_b32 v34, v240, v132, s42
	v_perm_b32 v35, v240, v132, s43
	v_perm_b32 v36, v240, v133, s42
	v_perm_b32 v37, v240, v133, s43
	v_pk_add_f16 v34, v34, s3 op_sel_hi:[1,0]
	v_pk_add_f16 v35, v35, s3 op_sel_hi:[1,0]
	v_pk_add_f16 v36, v36, s3 op_sel_hi:[1,0]
	v_pk_add_f16 v37, v37, s3 op_sel_hi:[1,0]
	s_waitcnt vmcnt(6)
	v_mfma_f32_32x32x16_f16 v[18:33], v[62:65], v[210:213], v[18:33]
	v_perm_b32 v132, v240, v152, s42
	v_perm_b32 v133, v240, v152, s43
	v_perm_b32 v134, v240, v153, s42
	v_perm_b32 v53, v240, v153, s43
	v_pk_add_f16 v50, v132, s3 op_sel_hi:[1,0]
	v_pk_add_f16 v51, v133, s3 op_sel_hi:[1,0]
	v_pk_add_f16 v52, v134, s3 op_sel_hi:[1,0]
	v_pk_add_f16 v53, v53, s3 op_sel_hi:[1,0]
	v_cvt_pk_f16_f32 v49, v48, v49
	v_cvt_pk_f16_f32 v48, v46, v47
	v_cvt_pk_f16_f32 v47, v44, v45
	v_cvt_pk_f16_f32 v46, v42, v43
	v_mfma_f32_32x32x16_f16 v[2:17], v[38:41], v[34:37], v[2:17]
	v_perm_b32 v42, v240, v130, s42
	v_perm_b32 v43, v240, v130, s43
	v_perm_b32 v44, v240, v131, s42
	v_perm_b32 v45, v240, v131, s43
	v_pk_add_f16 v42, v42, s3 op_sel_hi:[1,0]
	v_pk_add_f16 v43, v43, s3 op_sel_hi:[1,0]
	v_pk_add_f16 v44, v44, s3 op_sel_hi:[1,0]
	v_pk_add_f16 v45, v45, s3 op_sel_hi:[1,0]
	s_waitcnt vmcnt(5)
	v_mfma_f32_32x32x16_f16 v[18:33], v[38:41], v[50:53], v[18:33]
	v_perm_b32 v34, v240, v150, s42
	v_perm_b32 v35, v240, v150, s43
	v_perm_b32 v36, v240, v151, s42
	v_perm_b32 v37, v240, v151, s43
	v_pk_add_f16 v34, v34, s3 op_sel_hi:[1,0]
	v_pk_add_f16 v35, v35, s3 op_sel_hi:[1,0]
	v_pk_add_f16 v36, v36, s3 op_sel_hi:[1,0]
	v_pk_add_f16 v37, v37, s3 op_sel_hi:[1,0]
	v_mfma_f32_32x32x16_f16 v[2:17], v[46:49], v[42:45], v[2:17]
	global_load_dwordx2 v[154:155], v199, s[0:1] offset:2560
	global_load_dwordx2 v[152:153], v199, s[0:1] offset:3072
	global_load_dwordx2 v[150:151], v199, s[0:1] offset:3584
	s_or_b32 s0, s10, 6
	s_ashr_i32 s1, s0, 31
	s_lshl_b64 s[0:1], s[0:1], 12
	s_add_u32 s0, s8, s0
	v_mfma_f32_32x32x16_f16 v[18:33], v[46:49], v[34:37], v[18:33]
	s_nop 7
	s_nop 4
	v_cvt_pk_f16_f32 v254, v2, v3
	v_cvt_pk_f16_f32 v255, v4, v5
	ds_write_b64 v251, v[254:255] offset:18432
	v_pk_add_f32 v[222:223], v[222:223], v[2:3]
	v_pk_fma_f32 v[194:195], v[2:3], v[2:3], v[194:195]
	v_pk_add_f32 v[220:221], v[220:221], v[4:5]
	v_pk_fma_f32 v[192:193], v[4:5], v[4:5], v[192:193]
	v_cvt_pk_f16_f32 v252, v6, v7
	v_cvt_pk_f16_f32 v253, v8, v9
	ds_write_b64 v251, v[252:253] offset:18448
	v_pk_add_f32 v[218:219], v[218:219], v[6:7]
	v_pk_fma_f32 v[184:185], v[6:7], v[6:7], v[184:185]
	v_pk_add_f32 v[216:217], v[216:217], v[8:9]
	v_pk_fma_f32 v[166:167], v[8:9], v[8:9], v[166:167]
	v_cvt_pk_f16_f32 v254, v10, v11
	v_cvt_pk_f16_f32 v255, v12, v13
	ds_write_b64 v251, v[254:255] offset:18464
	v_pk_add_f32 v[214:215], v[214:215], v[10:11]
	v_pk_fma_f32 v[164:165], v[10:11], v[10:11], v[164:165]
	v_pk_add_f32 v[204:205], v[204:205], v[12:13]
	v_pk_fma_f32 v[162:163], v[12:13], v[12:13], v[162:163]
	v_cvt_pk_f16_f32 v252, v14, v15
	v_cvt_pk_f16_f32 v253, v16, v17
	ds_write_b64 v251, v[252:253] offset:18480
	v_pk_add_f32 v[202:203], v[202:203], v[14:15]
	v_pk_fma_f32 v[160:161], v[14:15], v[14:15], v[160:161]
	v_pk_add_f32 v[196:197], v[196:197], v[16:17]
	v_pk_fma_f32 v[156:157], v[16:17], v[16:17], v[156:157]
	v_cvt_pk_f16_f32 v254, v18, v19
	v_cvt_pk_f16_f32 v255, v20, v21
	ds_write_b64 v251, v[254:255] offset:23040
	v_pk_add_f32 v[222:223], v[222:223], v[18:19]
	v_pk_fma_f32 v[194:195], v[18:19], v[18:19], v[194:195]
	v_pk_add_f32 v[220:221], v[220:221], v[20:21]
	v_pk_fma_f32 v[192:193], v[20:21], v[20:21], v[192:193]
	v_cvt_pk_f16_f32 v252, v22, v23
	v_cvt_pk_f16_f32 v253, v24, v25
	ds_write_b64 v251, v[252:253] offset:23056
	v_pk_add_f32 v[218:219], v[218:219], v[22:23]
	v_pk_fma_f32 v[184:185], v[22:23], v[22:23], v[184:185]
	v_pk_add_f32 v[216:217], v[216:217], v[24:25]
	v_pk_fma_f32 v[166:167], v[24:25], v[24:25], v[166:167]
	v_cvt_pk_f16_f32 v254, v26, v27
	v_cvt_pk_f16_f32 v255, v28, v29
	ds_write_b64 v251, v[254:255] offset:23072
	v_pk_add_f32 v[214:215], v[214:215], v[26:27]
	v_pk_fma_f32 v[164:165], v[26:27], v[26:27], v[164:165]
	v_pk_add_f32 v[204:205], v[204:205], v[28:29]
	v_pk_fma_f32 v[162:163], v[28:29], v[28:29], v[162:163]
	v_cvt_pk_f16_f32 v252, v30, v31
	v_cvt_pk_f16_f32 v253, v32, v33
	ds_write_b64 v251, v[252:253] offset:23088
	v_pk_add_f32 v[202:203], v[202:203], v[30:31]
	v_pk_fma_f32 v[160:161], v[30:31], v[30:31], v[160:161]
	v_pk_add_f32 v[196:197], v[196:197], v[32:33]
	v_pk_fma_f32 v[156:157], v[32:33], v[32:33], v[156:157]
	s_nop 3
	s_nop 0
	s_nop 0
	s_waitcnt lgkmcnt(0)
	s_barrier
	ds_read_b128 v[2:5], v159
	s_nop 2
	ds_read_b128 v[18:21], v159 offset:8704
	s_waitcnt lgkmcnt(1)
	v_mfma_f32_32x32x16_f16 v[50:65], v[2:5], v[126:129], 0
	v_lshlrev_b32_e32 v0, 3, v0
	s_addc_u32 s1, s9, s1
	v_and_b32_e32 v0, 0x1f8, v0
	global_load_dwordx2 v[138:139], v0, s[0:1]
	s_waitcnt lgkmcnt(0)
	v_mfma_f32_32x32x16_f16 v[34:49], v[18:21], v[126:129], 0
	v_mfma_f32_32x32x16_f16 v[2:17], v[122:125], v[2:5], v[168:183]
	v_mfma_f32_32x32x16_f16 v[18:33], v[122:125], v[18:21], v[168:183]
	ds_read_b128 v[130:133], v159 offset:32
	ds_read_b128 v[134:137], v159 offset:8736
	s_waitcnt lgkmcnt(1)
	v_mfma_f32_32x32x16_f16 v[50:65], v[130:133], v[118:121], v[50:65]
	s_waitcnt lgkmcnt(0)
	v_mfma_f32_32x32x16_f16 v[34:49], v[134:137], v[118:121], v[34:49]
	v_mfma_f32_32x32x16_f16 v[2:17], v[114:117], v[130:133], v[2:17]
	v_mfma_f32_32x32x16_f16 v[18:33], v[114:117], v[134:137], v[18:33]
	ds_read_b128 v[224:227], v159 offset:64
	ds_read_b128 v[228:231], v159 offset:8768
	ds_read_b128 v[130:133], v159 offset:96
	ds_read_b128 v[134:137], v159 offset:8800
	s_waitcnt lgkmcnt(3)
	v_mfma_f32_32x32x16_f16 v[50:65], v[224:227], v[110:113], v[50:65]
	s_waitcnt lgkmcnt(2)
	v_mfma_f32_32x32x16_f16 v[34:49], v[228:231], v[110:113], v[34:49]
	v_mfma_f32_32x32x16_f16 v[2:17], v[106:109], v[224:227], v[2:17]
	v_mfma_f32_32x32x16_f16 v[18:33], v[106:109], v[228:231], v[18:33]
	ds_read_b128 v[224:227], v159 offset:128
	ds_read_b128 v[228:231], v159 offset:8832
	s_waitcnt lgkmcnt(3)
	v_mfma_f32_32x32x16_f16 v[50:65], v[130:133], v[102:105], v[50:65]
	s_waitcnt lgkmcnt(2)
	v_mfma_f32_32x32x16_f16 v[34:49], v[134:137], v[102:105], v[34:49]
	v_mfma_f32_32x32x16_f16 v[2:17], v[98:101], v[130:133], v[2:17]
	v_mfma_f32_32x32x16_f16 v[18:33], v[98:101], v[134:137], v[18:33]
	ds_read_b128 v[130:133], v159 offset:160
	ds_read_b128 v[134:137], v159 offset:8864
	s_waitcnt lgkmcnt(3)
	v_mfma_f32_32x32x16_f16 v[50:65], v[224:227], v[94:97], v[50:65]
	s_waitcnt lgkmcnt(2)
	v_mfma_f32_32x32x16_f16 v[34:49], v[228:231], v[94:97], v[34:49]
	v_mfma_f32_32x32x16_f16 v[2:17], v[86:89], v[224:227], v[2:17]
	v_mfma_f32_32x32x16_f16 v[18:33], v[86:89], v[228:231], v[18:33]
	ds_read_b128 v[224:227], v159 offset:192
	ds_read_b128 v[228:231], v159 offset:8896
	s_waitcnt lgkmcnt(3)
	v_mfma_f32_32x32x16_f16 v[50:65], v[130:133], v[90:93], v[50:65]
	s_waitcnt lgkmcnt(2)
	v_mfma_f32_32x32x16_f16 v[34:49], v[134:137], v[90:93], v[34:49]
	v_mfma_f32_32x32x16_f16 v[2:17], v[78:81], v[130:133], v[2:17]
	v_mfma_f32_32x32x16_f16 v[18:33], v[78:81], v[134:137], v[18:33]
	ds_read_b128 v[232:235], v159 offset:224
	ds_read_b128 v[236:239], v159 offset:8928
	s_waitcnt lgkmcnt(3)
	v_mfma_f32_32x32x16_f16 v[50:65], v[224:227], v[82:85], v[50:65]
	global_load_dwordx2 v[134:135], v0, s[0:1] offset:512
	global_load_dwordx2 v[132:133], v0, s[0:1] offset:1024
	global_load_dwordx2 v[130:131], v0, s[0:1] offset:1536
	s_waitcnt lgkmcnt(2)
	v_mfma_f32_32x32x16_f16 v[34:49], v[228:231], v[82:85], v[34:49]
	global_load_dwordx2 v[136:137], v0, s[0:1] offset:2048
	v_mfma_f32_32x32x16_f16 v[2:17], v[70:73], v[224:227], v[2:17]
	v_mfma_f32_32x32x16_f16 v[18:33], v[70:73], v[228:231], v[18:33]
	s_waitcnt lgkmcnt(1)
	v_mfma_f32_32x32x16_f16 v[50:65], v[232:235], v[74:77], v[50:65]
	v_mfma_f32_32x32x16_f16 v[2:17], v[66:69], v[232:235], v[2:17]
	s_nop 10
	v_cvt_pk_f16_f32 v57, v56, v57
	v_cvt_pk_f16_f32 v56, v54, v55
	v_cvt_pk_f16_f32 v54, v50, v51
	s_waitcnt vmcnt(12)
	v_lshlrev_b32_e32 v50, 8, v148
	v_cvt_pk_f16_f32 v55, v52, v53
	v_perm_b32 v50, v50, v148, s2
	v_lshrrev_b32_e32 v51, 16, v148
	v_lshrrev_b32_e32 v52, 8, v148
	v_lshrrev_b32_e32 v53, 16, v149
	v_lshrrev_b32_e32 v148, 8, v149
	v_perm_b32 v51, v52, v51, s2
	v_lshlrev_b32_e32 v52, 8, v149
	v_perm_b32 v53, v148, v53, s2
	s_waitcnt vmcnt(8)
	v_perm_b32 v52, v52, v149, s2
	v_perm_b32 v149, v240, v146, s43
	v_perm_b32 v198, v240, v147, s42
	s_waitcnt lgkmcnt(0)
	v_mfma_f32_32x32x16_f16 v[18:33], v[66:69], v[236:239], v[18:33]
	v_or_b32_e32 v50, 0x64006400, v50
	v_or_b32_e32 v51, 0x64006400, v51
	v_or_b32_e32 v52, 0x64006400, v52
	v_or_b32_e32 v53, 0x64006400, v53
	v_pk_add_f16 v50, v50, s3 op_sel_hi:[1,0]
	v_pk_add_f16 v51, v51, s3 op_sel_hi:[1,0]
	v_pk_add_f16 v52, v52, s3 op_sel_hi:[1,0]
	v_pk_add_f16 v53, v53, s3 op_sel_hi:[1,0]
	v_perm_b32 v148, v240, v146, s42
	v_perm_b32 v200, v240, v147, s43
	v_pk_add_f16 v146, v148, s3 op_sel_hi:[1,0]
	v_pk_add_f16 v147, v149, s3 op_sel_hi:[1,0]
	v_pk_add_f16 v148, v198, s3 op_sel_hi:[1,0]
	v_pk_add_f16 v149, v200, s3 op_sel_hi:[1,0]
	v_cvt_pk_f16_f32 v65, v64, v65
	v_cvt_pk_f16_f32 v64, v62, v63
	v_cvt_pk_f16_f32 v62, v58, v59
	v_cvt_pk_f16_f32 v63, v60, v61
	s_waitcnt vmcnt(7)
	v_mfma_f32_32x32x16_f16 v[34:49], v[236:239], v[74:77], v[34:49]
	v_mfma_f32_32x32x16_f16 v[2:17], v[54:57], v[50:53], v[2:17]
	v_perm_b32 v58, v240, v144, s42
	v_perm_b32 v59, v240, v144, s43
	v_perm_b32 v60, v240, v145, s42
	v_perm_b32 v61, v240, v145, s43
	v_mfma_f32_32x32x16_f16 v[18:33], v[54:57], v[146:149], v[18:33]
	v_pk_add_f16 v58, v58, s3 op_sel_hi:[1,0]
	v_pk_add_f16 v59, v59, s3 op_sel_hi:[1,0]
	v_pk_add_f16 v60, v60, s3 op_sel_hi:[1,0]
	v_pk_add_f16 v61, v61, s3 op_sel_hi:[1,0]
	v_perm_b32 v144, v240, v154, s42
	v_perm_b32 v145, v240, v154, s43
	v_perm_b32 v154, v240, v155, s42
	v_perm_b32 v155, v240, v155, s43
	v_pk_add_f16 v224, v144, s3 op_sel_hi:[1,0]
	v_pk_add_f16 v225, v145, s3 op_sel_hi:[1,0]
	v_pk_add_f16 v226, v154, s3 op_sel_hi:[1,0]
	v_pk_add_f16 v227, v155, s3 op_sel_hi:[1,0]
	v_cvt_pk_f16_f32 v41, v40, v41
	v_cvt_pk_f16_f32 v40, v38, v39
	v_cvt_pk_f16_f32 v39, v36, v37
	v_cvt_pk_f16_f32 v38, v34, v35
	s_waitcnt vmcnt(6)
	v_mfma_f32_32x32x16_f16 v[2:17], v[62:65], v[58:61], v[2:17]
	v_perm_b32 v34, v240, v142, s42
	v_perm_b32 v35, v240, v142, s43
	v_mfma_f32_32x32x16_f16 v[18:33], v[62:65], v[224:227], v[18:33]
	v_perm_b32 v36, v240, v143, s42
	v_perm_b32 v37, v240, v143, s43
	v_pk_add_f16 v34, v34, s3 op_sel_hi:[1,0]
	v_pk_add_f16 v35, v35, s3 op_sel_hi:[1,0]
	v_pk_add_f16 v36, v36, s3 op_sel_hi:[1,0]
	v_pk_add_f16 v37, v37, s3 op_sel_hi:[1,0]
	v_perm_b32 v142, v240, v152, s42
	v_perm_b32 v143, v240, v152, s43
	v_perm_b32 v144, v240, v153, s42
	v_perm_b32 v53, v240, v153, s43
	v_pk_add_f16 v50, v142, s3 op_sel_hi:[1,0]
	v_pk_add_f16 v51, v143, s3 op_sel_hi:[1,0]
	v_pk_add_f16 v52, v144, s3 op_sel_hi:[1,0]
	v_pk_add_f16 v53, v53, s3 op_sel_hi:[1,0]
	v_cvt_pk_f16_f32 v49, v48, v49
	v_cvt_pk_f16_f32 v48, v46, v47
	v_cvt_pk_f16_f32 v47, v44, v45
	v_cvt_pk_f16_f32 v46, v42, v43
	v_mfma_f32_32x32x16_f16 v[2:17], v[38:41], v[34:37], v[2:17]
	s_waitcnt vmcnt(5)
	v_mfma_f32_32x32x16_f16 v[18:33], v[38:41], v[50:53], v[18:33]
	v_perm_b32 v42, v240, v140, s42
	v_perm_b32 v43, v240, v140, s43
	v_perm_b32 v44, v240, v141, s42
	v_perm_b32 v45, v240, v141, s43
	v_perm_b32 v34, v240, v150, s42
	v_perm_b32 v35, v240, v150, s43
	v_perm_b32 v36, v240, v151, s42
	v_perm_b32 v37, v240, v151, s43
	v_pk_add_f16 v42, v42, s3 op_sel_hi:[1,0]
	v_pk_add_f16 v43, v43, s3 op_sel_hi:[1,0]
	v_pk_add_f16 v44, v44, s3 op_sel_hi:[1,0]
	v_pk_add_f16 v45, v45, s3 op_sel_hi:[1,0]
	v_pk_add_f16 v34, v34, s3 op_sel_hi:[1,0]
	v_pk_add_f16 v35, v35, s3 op_sel_hi:[1,0]
	v_pk_add_f16 v36, v36, s3 op_sel_hi:[1,0]
	v_pk_add_f16 v37, v37, s3 op_sel_hi:[1,0]
	v_mfma_f32_32x32x16_f16 v[2:17], v[46:49], v[42:45], v[2:17]
	global_load_dwordx2 v[142:143], v0, s[0:1] offset:2560
	global_load_dwordx2 v[140:141], v0, s[0:1] offset:3072
	global_load_dwordx2 v[64:65], v0, s[0:1] offset:3584
	v_mfma_f32_32x32x16_f16 v[18:33], v[46:49], v[34:37], v[18:33]
	s_nop 7
	s_nop 4
	v_cvt_pk_f16_f32 v254, v2, v3
	v_cvt_pk_f16_f32 v255, v4, v5
	ds_write_b64 v251, v[254:255] offset:0
	v_pk_add_f32 v[222:223], v[222:223], v[2:3]
	v_pk_fma_f32 v[194:195], v[2:3], v[2:3], v[194:195]
	v_pk_add_f32 v[220:221], v[220:221], v[4:5]
	v_pk_fma_f32 v[192:193], v[4:5], v[4:5], v[192:193]
	v_cvt_pk_f16_f32 v252, v6, v7
	v_cvt_pk_f16_f32 v253, v8, v9
	ds_write_b64 v251, v[252:253] offset:16
	v_pk_add_f32 v[218:219], v[218:219], v[6:7]
	v_pk_fma_f32 v[184:185], v[6:7], v[6:7], v[184:185]
	v_pk_add_f32 v[216:217], v[216:217], v[8:9]
	v_pk_fma_f32 v[166:167], v[8:9], v[8:9], v[166:167]
	v_cvt_pk_f16_f32 v254, v10, v11
	v_cvt_pk_f16_f32 v255, v12, v13
	ds_write_b64 v251, v[254:255] offset:32
	v_pk_add_f32 v[214:215], v[214:215], v[10:11]
	v_pk_fma_f32 v[164:165], v[10:11], v[10:11], v[164:165]
	v_pk_add_f32 v[204:205], v[204:205], v[12:13]
	v_pk_fma_f32 v[162:163], v[12:13], v[12:13], v[162:163]
	v_cvt_pk_f16_f32 v252, v14, v15
	v_cvt_pk_f16_f32 v253, v16, v17
	ds_write_b64 v251, v[252:253] offset:48
	v_pk_add_f32 v[202:203], v[202:203], v[14:15]
	v_pk_fma_f32 v[160:161], v[14:15], v[14:15], v[160:161]
	v_pk_add_f32 v[196:197], v[196:197], v[16:17]
	v_pk_fma_f32 v[156:157], v[16:17], v[16:17], v[156:157]
	v_cvt_pk_f16_f32 v254, v18, v19
	v_cvt_pk_f16_f32 v255, v20, v21
	ds_write_b64 v251, v[254:255] offset:4608
	v_pk_add_f32 v[222:223], v[222:223], v[18:19]
	v_pk_fma_f32 v[194:195], v[18:19], v[18:19], v[194:195]
	v_pk_add_f32 v[220:221], v[220:221], v[20:21]
	v_pk_fma_f32 v[192:193], v[20:21], v[20:21], v[192:193]
	v_cvt_pk_f16_f32 v252, v22, v23
	v_cvt_pk_f16_f32 v253, v24, v25
	ds_write_b64 v251, v[252:253] offset:4624
	v_pk_add_f32 v[218:219], v[218:219], v[22:23]
	v_pk_fma_f32 v[184:185], v[22:23], v[22:23], v[184:185]
	v_pk_add_f32 v[216:217], v[216:217], v[24:25]
	v_pk_fma_f32 v[166:167], v[24:25], v[24:25], v[166:167]
	v_cvt_pk_f16_f32 v254, v26, v27
	v_cvt_pk_f16_f32 v255, v28, v29
	ds_write_b64 v251, v[254:255] offset:4640
	v_pk_add_f32 v[214:215], v[214:215], v[26:27]
	v_pk_fma_f32 v[164:165], v[26:27], v[26:27], v[164:165]
	v_pk_add_f32 v[204:205], v[204:205], v[28:29]
	v_pk_fma_f32 v[162:163], v[28:29], v[28:29], v[162:163]
	v_cvt_pk_f16_f32 v252, v30, v31
	v_cvt_pk_f16_f32 v253, v32, v33
	ds_write_b64 v251, v[252:253] offset:4656
	v_pk_add_f32 v[202:203], v[202:203], v[30:31]
	v_pk_fma_f32 v[160:161], v[30:31], v[30:31], v[160:161]
	v_pk_add_f32 v[196:197], v[196:197], v[32:33]
	v_pk_fma_f32 v[156:157], v[32:33], v[32:33], v[156:157]
	s_nop 7
	s_waitcnt lgkmcnt(0)
	s_barrier
	s_nop 1
	ds_read_b128 v[16:19], v159 offset:43520
	s_waitcnt lgkmcnt(0)
	v_mfma_f32_32x32x16_f16 v[32:47], v[16:19], v[126:129], 0
	ds_read_b128 v[2:5], v159 offset:34816
	s_waitcnt lgkmcnt(0)
	v_mfma_f32_32x32x16_f16 v[48:63], v[2:5], v[126:129], 0
	ds_read_b128 v[126:129], v159 offset:34848
	s_waitcnt lgkmcnt(0)
	v_mfma_f32_32x32x16_f16 v[48:63], v[126:129], v[118:121], v[48:63]
	v_mfma_f32_32x32x16_f16 v[0:15], v[122:125], v[2:5], v[168:183]
	v_mfma_f32_32x32x16_f16 v[0:15], v[114:117], v[126:129], v[0:15]
	v_mfma_f32_32x32x16_f16 v[16:31], v[122:125], v[16:19], v[168:183]
	ds_read_b128 v[122:125], v159 offset:43552
	s_waitcnt lgkmcnt(0)
	v_mfma_f32_32x32x16_f16 v[32:47], v[122:125], v[118:121], v[32:47]
	v_mfma_f32_32x32x16_f16 v[16:31], v[114:117], v[122:125], v[16:31]
	ds_read_b128 v[118:121], v159 offset:34880
	ds_read_b128 v[114:117], v159 offset:43584
	s_waitcnt lgkmcnt(1)
	v_mfma_f32_32x32x16_f16 v[48:63], v[118:121], v[110:113], v[48:63]
	s_waitcnt lgkmcnt(0)
	v_mfma_f32_32x32x16_f16 v[32:47], v[114:117], v[110:113], v[32:47]
	v_mfma_f32_32x32x16_f16 v[0:15], v[106:109], v[118:121], v[0:15]
	ds_read_b128 v[110:113], v159 offset:34912
	v_mfma_f32_32x32x16_f16 v[16:31], v[106:109], v[114:117], v[16:31]
	ds_read_b128 v[106:109], v159 offset:43616
	s_waitcnt lgkmcnt(1)
	v_mfma_f32_32x32x16_f16 v[48:63], v[110:113], v[102:105], v[48:63]
	s_waitcnt lgkmcnt(0)
	v_mfma_f32_32x32x16_f16 v[32:47], v[106:109], v[102:105], v[32:47]
	v_mfma_f32_32x32x16_f16 v[0:15], v[98:101], v[110:113], v[0:15]
	ds_read_b128 v[102:105], v159 offset:34944
	v_mfma_f32_32x32x16_f16 v[16:31], v[98:101], v[106:109], v[16:31]
	ds_read_b128 v[98:101], v159 offset:43648
	s_waitcnt lgkmcnt(1)
	v_mfma_f32_32x32x16_f16 v[48:63], v[102:105], v[94:97], v[48:63]
	s_waitcnt lgkmcnt(0)
	v_mfma_f32_32x32x16_f16 v[32:47], v[98:101], v[94:97], v[32:47]
	v_mfma_f32_32x32x16_f16 v[0:15], v[86:89], v[102:105], v[0:15]
	ds_read_b128 v[94:97], v159 offset:34976
	v_mfma_f32_32x32x16_f16 v[16:31], v[86:89], v[98:101], v[16:31]
	ds_read_b128 v[86:89], v159 offset:43680
	s_waitcnt lgkmcnt(1)
	v_mfma_f32_32x32x16_f16 v[48:63], v[94:97], v[90:93], v[48:63]
	s_waitcnt lgkmcnt(0)
	v_mfma_f32_32x32x16_f16 v[32:47], v[86:89], v[90:93], v[32:47]
	v_mfma_f32_32x32x16_f16 v[0:15], v[78:81], v[94:97], v[0:15]
	ds_read_b128 v[90:93], v159 offset:35008
	v_mfma_f32_32x32x16_f16 v[16:31], v[78:81], v[86:89], v[16:31]
	ds_read_b128 v[78:81], v159 offset:43712
	s_waitcnt lgkmcnt(1)
	v_mfma_f32_32x32x16_f16 v[48:63], v[90:93], v[82:85], v[48:63]
	s_waitcnt lgkmcnt(0)
	v_mfma_f32_32x32x16_f16 v[32:47], v[78:81], v[82:85], v[32:47]
	v_mfma_f32_32x32x16_f16 v[0:15], v[70:73], v[90:93], v[0:15]
	ds_read_b128 v[82:85], v159 offset:35040
	v_mfma_f32_32x32x16_f16 v[16:31], v[70:73], v[78:81], v[16:31]
	ds_read_b128 v[70:73], v159 offset:43744
	s_waitcnt lgkmcnt(1)
	v_mfma_f32_32x32x16_f16 v[48:63], v[82:85], v[74:77], v[48:63]
	v_mfma_f32_32x32x16_f16 v[0:15], v[66:69], v[82:85], v[0:15]
	s_nop 3
	s_nop 6
	v_cvt_pk_f16_f32 v55, v54, v55
	v_cvt_pk_f16_f32 v54, v52, v53
	v_cvt_pk_f16_f32 v53, v50, v51
	v_cvt_pk_f16_f32 v52, v48, v49
	s_waitcnt vmcnt(3)
	s_waitcnt lgkmcnt(0)
	v_mfma_f32_32x32x16_f16 v[16:31], v[66:69], v[70:73], v[16:31]
	v_lshrrev_b32_e32 v69, 16, v139
	v_mfma_f32_32x32x16_f16 v[32:47], v[70:73], v[74:77], v[32:47]
	v_lshrrev_b32_e32 v70, 8, v139
	v_perm_b32 v69, v70, v69, s2
	v_perm_b32 v66, v240, v138, s42
	v_perm_b32 v67, v240, v138, s43
	v_perm_b32 v68, v240, v139, s42
	v_or_b32_e32 v69, 0x64006400, v69
	v_pk_add_f16 v66, v66, s3 op_sel_hi:[1,0]
	v_pk_add_f16 v67, v67, s3 op_sel_hi:[1,0]
	v_pk_add_f16 v68, v68, s3 op_sel_hi:[1,0]
	v_pk_add_f16 v69, v69, s3 op_sel_hi:[1,0]
	s_nop 1
	v_mfma_f32_32x32x16_f16 v[0:15], v[52:55], v[66:69], v[0:15]
	v_perm_b32 v48, v240, v136, s42
	v_perm_b32 v49, v240, v136, s43
	v_perm_b32 v50, v240, v137, s42
	v_perm_b32 v51, v240, v137, s43
	v_pk_add_f16 v48, v48, s3 op_sel_hi:[1,0]
	v_pk_add_f16 v49, v49, s3 op_sel_hi:[1,0]
	v_pk_add_f16 v50, v50, s3 op_sel_hi:[1,0]
	v_pk_add_f16 v51, v51, s3 op_sel_hi:[1,0]
	v_cvt_pk_f16_f32 v39, v38, v39
	v_cvt_pk_f16_f32 v38, v36, v37
	v_mfma_f32_32x32x16_f16 v[16:31], v[52:55], v[48:51], v[16:31]
	v_perm_b32 v48, v240, v134, s42
	v_perm_b32 v49, v240, v134, s43
	v_perm_b32 v50, v240, v135, s42
	v_perm_b32 v51, v240, v135, s43
	v_pk_add_f16 v48, v48, s3 op_sel_hi:[1,0]
	v_pk_add_f16 v49, v49, s3 op_sel_hi:[1,0]
	v_pk_add_f16 v50, v50, s3 op_sel_hi:[1,0]
	v_pk_add_f16 v51, v51, s3 op_sel_hi:[1,0]
	v_cvt_pk_f16_f32 v55, v62, v63
	v_cvt_pk_f16_f32 v54, v60, v61
	v_cvt_pk_f16_f32 v53, v58, v59
	v_cvt_pk_f16_f32 v52, v56, v57
	s_waitcnt vmcnt(2)
	v_cvt_pk_f16_f32 v37, v34, v35
	v_mfma_f32_32x32x16_f16 v[0:15], v[52:55], v[48:51], v[0:15]
	v_perm_b32 v48, v240, v142, s42
	v_perm_b32 v49, v240, v142, s43
	v_perm_b32 v50, v240, v143, s42
	v_perm_b32 v51, v240, v143, s43
	v_pk_add_f16 v48, v48, s3 op_sel_hi:[1,0]
	v_pk_add_f16 v49, v49, s3 op_sel_hi:[1,0]
	v_pk_add_f16 v50, v50, s3 op_sel_hi:[1,0]
	v_pk_add_f16 v51, v51, s3 op_sel_hi:[1,0]
	v_cvt_pk_f16_f32 v36, v32, v33
	s_waitcnt vmcnt(1)
	v_mfma_f32_32x32x16_f16 v[16:31], v[52:55], v[48:51], v[16:31]
	v_lshrrev_b32_e32 v51, 16, v133
	v_lshrrev_b32_e32 v52, 8, v133
	v_perm_b32 v51, v52, v51, s2
	v_perm_b32 v48, v240, v132, s42
	v_perm_b32 v49, v240, v132, s43
	v_perm_b32 v50, v240, v133, s42
	v_or_b32_e32 v51, 0x64006400, v51
	v_pk_add_f16 v48, v48, s3 op_sel_hi:[1,0]
	v_pk_add_f16 v49, v49, s3 op_sel_hi:[1,0]
	v_pk_add_f16 v50, v50, s3 op_sel_hi:[1,0]
	v_pk_add_f16 v51, v51, s3 op_sel_hi:[1,0]
	s_nop 1
	v_mfma_f32_32x32x16_f16 v[0:15], v[36:39], v[48:51], v[0:15]
	v_perm_b32 v32, v240, v140, s42
	v_perm_b32 v33, v240, v140, s43
	v_perm_b32 v34, v240, v141, s42
	v_perm_b32 v35, v240, v141, s43
	v_pk_add_f16 v32, v32, s3 op_sel_hi:[1,0]
	v_pk_add_f16 v33, v33, s3 op_sel_hi:[1,0]
	v_pk_add_f16 v34, v34, s3 op_sel_hi:[1,0]
	v_pk_add_f16 v35, v35, s3 op_sel_hi:[1,0]
	s_nop 1
	v_mfma_f32_32x32x16_f16 v[16:31], v[36:39], v[32:35], v[16:31]
	v_perm_b32 v32, v240, v130, s42
	v_perm_b32 v33, v240, v130, s43
	v_perm_b32 v34, v240, v131, s42
	v_perm_b32 v35, v240, v131, s43
	v_pk_add_f16 v32, v32, s3 op_sel_hi:[1,0]
	v_pk_add_f16 v33, v33, s3 op_sel_hi:[1,0]
	v_pk_add_f16 v34, v34, s3 op_sel_hi:[1,0]
	v_pk_add_f16 v35, v35, s3 op_sel_hi:[1,0]
	v_cvt_pk_f16_f32 v39, v46, v47
	v_cvt_pk_f16_f32 v38, v44, v45
	v_cvt_pk_f16_f32 v37, v42, v43
	v_cvt_pk_f16_f32 v36, v40, v41
	s_waitcnt vmcnt(0)
	s_nop 0
	v_mfma_f32_32x32x16_f16 v[0:15], v[36:39], v[32:35], v[0:15]
	v_perm_b32 v32, v240, v64, s42
	v_perm_b32 v33, v240, v64, s43
	v_perm_b32 v34, v240, v65, s42
	v_perm_b32 v35, v240, v65, s43
	v_pk_add_f16 v32, v32, s3 op_sel_hi:[1,0]
	v_pk_add_f16 v33, v33, s3 op_sel_hi:[1,0]
	v_pk_add_f16 v34, v34, s3 op_sel_hi:[1,0]
	v_pk_add_f16 v35, v35, s3 op_sel_hi:[1,0]
	s_nop 3
	v_mfma_f32_32x32x16_f16 v[16:31], v[36:39], v[32:35], v[16:31]
	s_nop 7
	s_nop 4
	v_cvt_pk_f16_f32 v254, v0, v1
	v_cvt_pk_f16_f32 v255, v2, v3
	ds_write_b64 v251, v[254:255] offset:18432
	v_pk_add_f32 v[222:223], v[222:223], v[0:1]
	v_pk_fma_f32 v[194:195], v[0:1], v[0:1], v[194:195]
	v_pk_add_f32 v[220:221], v[220:221], v[2:3]
	v_pk_fma_f32 v[192:193], v[2:3], v[2:3], v[192:193]
	v_cvt_pk_f16_f32 v252, v4, v5
	v_cvt_pk_f16_f32 v253, v6, v7
	ds_write_b64 v251, v[252:253] offset:18448
	v_pk_add_f32 v[218:219], v[218:219], v[4:5]
	v_pk_fma_f32 v[184:185], v[4:5], v[4:5], v[184:185]
	v_pk_add_f32 v[216:217], v[216:217], v[6:7]
	v_pk_fma_f32 v[166:167], v[6:7], v[6:7], v[166:167]
	v_cvt_pk_f16_f32 v254, v8, v9
	v_cvt_pk_f16_f32 v255, v10, v11
	ds_write_b64 v251, v[254:255] offset:18464
	v_pk_add_f32 v[214:215], v[214:215], v[8:9]
	v_pk_fma_f32 v[164:165], v[8:9], v[8:9], v[164:165]
	v_pk_add_f32 v[204:205], v[204:205], v[10:11]
	v_pk_fma_f32 v[162:163], v[10:11], v[10:11], v[162:163]
	v_cvt_pk_f16_f32 v252, v12, v13
	v_cvt_pk_f16_f32 v253, v14, v15
	ds_write_b64 v251, v[252:253] offset:18480
	v_pk_add_f32 v[202:203], v[202:203], v[12:13]
	v_pk_fma_f32 v[160:161], v[12:13], v[12:13], v[160:161]
	v_pk_add_f32 v[196:197], v[196:197], v[14:15]
	v_pk_fma_f32 v[156:157], v[14:15], v[14:15], v[156:157]
	v_cvt_pk_f16_f32 v254, v16, v17
	v_cvt_pk_f16_f32 v255, v18, v19
	ds_write_b64 v251, v[254:255] offset:23040
	v_pk_add_f32 v[222:223], v[222:223], v[16:17]
	v_pk_fma_f32 v[194:195], v[16:17], v[16:17], v[194:195]
	v_pk_add_f32 v[220:221], v[220:221], v[18:19]
	v_pk_fma_f32 v[192:193], v[18:19], v[18:19], v[192:193]
	v_cvt_pk_f16_f32 v252, v20, v21
	v_cvt_pk_f16_f32 v253, v22, v23
	ds_write_b64 v251, v[252:253] offset:23056
	v_pk_add_f32 v[218:219], v[218:219], v[20:21]
	v_pk_fma_f32 v[184:185], v[20:21], v[20:21], v[184:185]
	v_pk_add_f32 v[216:217], v[216:217], v[22:23]
	v_pk_fma_f32 v[166:167], v[22:23], v[22:23], v[166:167]
	v_cvt_pk_f16_f32 v254, v24, v25
	v_cvt_pk_f16_f32 v255, v26, v27
	ds_write_b64 v251, v[254:255] offset:23072
	v_pk_add_f32 v[214:215], v[214:215], v[24:25]
	v_pk_fma_f32 v[164:165], v[24:25], v[24:25], v[164:165]
	v_pk_add_f32 v[204:205], v[204:205], v[26:27]
	v_pk_fma_f32 v[162:163], v[26:27], v[26:27], v[162:163]
	v_cvt_pk_f16_f32 v252, v28, v29
	v_cvt_pk_f16_f32 v253, v30, v31
	ds_write_b64 v251, v[252:253] offset:23088
	v_pk_add_f32 v[202:203], v[202:203], v[28:29]
	v_pk_fma_f32 v[160:161], v[28:29], v[28:29], v[160:161]
	v_pk_add_f32 v[196:197], v[196:197], v[30:31]
	v_pk_fma_f32 v[156:157], v[30:31], v[30:31], v[156:157]
	s_nop 4
	s_nop 0
	v_add_f32_dpp v222, v222, v222 row_half_mirror row_mask:0xf bank_mask:0x5
	v_add_f32_dpp v222, v223, v223 row_half_mirror row_mask:0xf bank_mask:0xa
	v_add_f32_dpp v220, v220, v220 row_half_mirror row_mask:0xf bank_mask:0x5
	v_add_f32_dpp v220, v221, v221 row_half_mirror row_mask:0xf bank_mask:0xa
	v_add_f32_dpp v218, v218, v218 row_half_mirror row_mask:0xf bank_mask:0x5
	v_add_f32_dpp v218, v219, v219 row_half_mirror row_mask:0xf bank_mask:0xa
	v_add_f32_dpp v216, v216, v216 row_half_mirror row_mask:0xf bank_mask:0x5
	v_add_f32_dpp v216, v217, v217 row_half_mirror row_mask:0xf bank_mask:0xa
	v_add_f32_dpp v214, v214, v214 row_half_mirror row_mask:0xf bank_mask:0x5
	v_add_f32_dpp v214, v215, v215 row_half_mirror row_mask:0xf bank_mask:0xa
	v_add_f32_dpp v204, v204, v204 row_half_mirror row_mask:0xf bank_mask:0x5
	v_add_f32_dpp v204, v205, v205 row_half_mirror row_mask:0xf bank_mask:0xa
	v_add_f32_dpp v202, v202, v202 row_half_mirror row_mask:0xf bank_mask:0x5
	v_add_f32_dpp v202, v203, v203 row_half_mirror row_mask:0xf bank_mask:0xa
	v_add_f32_dpp v196, v196, v196 row_half_mirror row_mask:0xf bank_mask:0x5
	v_add_f32_dpp v196, v197, v197 row_half_mirror row_mask:0xf bank_mask:0xa
	v_add_f32_dpp v194, v194, v194 row_half_mirror row_mask:0xf bank_mask:0x5
	v_add_f32_dpp v194, v195, v195 row_half_mirror row_mask:0xf bank_mask:0xa
	v_add_f32_dpp v192, v192, v192 row_half_mirror row_mask:0xf bank_mask:0x5
	v_add_f32_dpp v192, v193, v193 row_half_mirror row_mask:0xf bank_mask:0xa
	v_add_f32_dpp v184, v184, v184 row_half_mirror row_mask:0xf bank_mask:0x5
	v_add_f32_dpp v184, v185, v185 row_half_mirror row_mask:0xf bank_mask:0xa
	v_add_f32_dpp v166, v166, v166 row_half_mirror row_mask:0xf bank_mask:0x5
	v_add_f32_dpp v166, v167, v167 row_half_mirror row_mask:0xf bank_mask:0xa
	v_add_f32_dpp v164, v164, v164 row_half_mirror row_mask:0xf bank_mask:0x5
	v_add_f32_dpp v164, v165, v165 row_half_mirror row_mask:0xf bank_mask:0xa
	v_add_f32_dpp v162, v162, v162 row_half_mirror row_mask:0xf bank_mask:0x5
	v_add_f32_dpp v162, v163, v163 row_half_mirror row_mask:0xf bank_mask:0xa
	v_add_f32_dpp v160, v160, v160 row_half_mirror row_mask:0xf bank_mask:0x5
	v_add_f32_dpp v160, v161, v161 row_half_mirror row_mask:0xf bank_mask:0xa
	v_add_f32_dpp v156, v156, v156 row_half_mirror row_mask:0xf bank_mask:0x5
	v_add_f32_dpp v156, v157, v157 row_half_mirror row_mask:0xf bank_mask:0xa
	v_add_f32_dpp v222, v222, v222 row_ror:8 row_mask:0xf bank_mask:0x3
	v_add_f32_dpp v222, v220, v220 row_ror:8 row_mask:0xf bank_mask:0xc
	v_add_f32_dpp v218, v218, v218 row_ror:8 row_mask:0xf bank_mask:0x3
	v_add_f32_dpp v218, v216, v216 row_ror:8 row_mask:0xf bank_mask:0xc
	v_add_f32_dpp v214, v214, v214 row_ror:8 row_mask:0xf bank_mask:0x3
	v_add_f32_dpp v214, v204, v204 row_ror:8 row_mask:0xf bank_mask:0xc
	v_add_f32_dpp v202, v202, v202 row_ror:8 row_mask:0xf bank_mask:0x3
	v_add_f32_dpp v202, v196, v196 row_ror:8 row_mask:0xf bank_mask:0xc
	v_add_f32_dpp v194, v194, v194 row_ror:8 row_mask:0xf bank_mask:0x3
	v_add_f32_dpp v194, v192, v192 row_ror:8 row_mask:0xf bank_mask:0xc
	v_add_f32_dpp v184, v184, v184 row_ror:8 row_mask:0xf bank_mask:0x3
	v_add_f32_dpp v184, v166, v166 row_ror:8 row_mask:0xf bank_mask:0xc
	v_add_f32_dpp v164, v164, v164 row_ror:8 row_mask:0xf bank_mask:0x3
	v_add_f32_dpp v164, v162, v162 row_ror:8 row_mask:0xf bank_mask:0xc
	v_add_f32_dpp v160, v160, v160 row_ror:8 row_mask:0xf bank_mask:0x3
	v_add_f32_dpp v160, v156, v156 row_ror:8 row_mask:0xf bank_mask:0xc
	v_add_f32_dpp v222, v222, v222 quad_perm:[1,0,3,2] row_mask:0xf bank_mask:0xf
	v_add_f32_dpp v218, v218, v218 quad_perm:[1,0,3,2] row_mask:0xf bank_mask:0xf
	v_add_f32_dpp v214, v214, v214 quad_perm:[1,0,3,2] row_mask:0xf bank_mask:0xf
	v_add_f32_dpp v202, v202, v202 quad_perm:[1,0,3,2] row_mask:0xf bank_mask:0xf
	v_add_f32_dpp v194, v194, v194 quad_perm:[1,0,3,2] row_mask:0xf bank_mask:0xf
	v_add_f32_dpp v184, v184, v184 quad_perm:[1,0,3,2] row_mask:0xf bank_mask:0xf
	v_add_f32_dpp v164, v164, v164 quad_perm:[1,0,3,2] row_mask:0xf bank_mask:0xf
	v_add_f32_dpp v160, v160, v160 quad_perm:[1,0,3,2] row_mask:0xf bank_mask:0xf
	v_add_f32_dpp v222, v222, v222 quad_perm:[2,3,0,1] row_mask:0xf bank_mask:0xf
	v_add_f32_dpp v218, v218, v218 quad_perm:[2,3,0,1] row_mask:0xf bank_mask:0xf
	v_add_f32_dpp v214, v214, v214 quad_perm:[2,3,0,1] row_mask:0xf bank_mask:0xf
	v_add_f32_dpp v202, v202, v202 quad_perm:[2,3,0,1] row_mask:0xf bank_mask:0xf
	v_add_f32_dpp v194, v194, v194 quad_perm:[2,3,0,1] row_mask:0xf bank_mask:0xf
	v_add_f32_dpp v184, v184, v184 quad_perm:[2,3,0,1] row_mask:0xf bank_mask:0xf
	v_add_f32_dpp v164, v164, v164 quad_perm:[2,3,0,1] row_mask:0xf bank_mask:0xf
	v_add_f32_dpp v160, v160, v160 quad_perm:[2,3,0,1] row_mask:0xf bank_mask:0xf
	s_mov_b32 exec_lo, 0x11111111
	s_mov_b32 exec_hi, 0x11111111
	ds_add_f32 v250, v222 offset:0
	ds_add_f32 v250, v218 offset:32
	ds_add_f32 v250, v214 offset:64
	ds_add_f32 v250, v202 offset:96
	ds_add_f32 v250, v194 offset:256
	ds_add_f32 v250, v184 offset:288
	ds_add_f32 v250, v164 offset:320
	ds_add_f32 v250, v160 offset:352
	s_mov_b64 exec, -1
	s_waitcnt lgkmcnt(0)
	s_barrier
	s_cmp_lg_u32 s50, 0
	s_cbranch_scc1 .LBB3_27
	v_mbcnt_lo_u32_b32 v2, -1, 0
	v_mbcnt_hi_u32_b32 v2, -1, v2
	v_and_b32_e32 v3, 32, v2
	v_add_u32_e32 v4, v2, v3
	v_lshl_add_u32 v5, v4, 2, s49
	ds_read_b32 v6, v5
	v_lshl_add_u32 v4, v3, 1, v4
	v_add_u32_e32 v4, s48, v4
	v_lshlrev_b32_e32 v4, 2, v4
	s_waitcnt lgkmcnt(0)
	global_atomic_add_f32 v4, v6, s[46:47]
